# s11
# speedup vs baseline: 1.0500x; 1.0065x over previous
.LBB1_5:
	v_lshlrev_b32_e32 v67, 4, v1
	v_lshrrev_b32_e32 v1, 1, v1
	v_lshrrev_b32_e32 v69, 5, v132
	v_ashrrev_i32_e32 v66, 4, v132
	v_bitop3_b32 v1, v1, v69, 7 bitop3:0x78
	s_add_u32 s22, s24, s2
	v_lshlrev_b32_e32 v68, 7, v66
	v_lshlrev_b32_e32 v1, 4, v1
	v_and_b32_e32 v0, 8, v0
	s_addc_u32 s90, s25, s3
	v_lshl_or_b32 v201, v66, 12, v67
	v_or3_b32 v0, v68, v1, v0
	v_add_u32_e32 v100, 0x10000, v0
	v_cvt_pk_f16_f32 v1, v64, v65
	v_cvt_pk_f16_f32 v0, v62, v63
	v_cvt_pk_f16_f32 v61, v60, v61
	v_cvt_pk_f16_f32 v60, v58, v59
	ds_write2st64_b64 v100, v[0:1], v[60:61] offset1:8
	v_cvt_pk_f16_f32 v1, v56, v57
	v_cvt_pk_f16_f32 v0, v54, v55
	v_cvt_pk_f16_f32 v53, v52, v53
	v_cvt_pk_f16_f32 v52, v50, v51
	ds_write2st64_b64 v100, v[0:1], v[52:53] offset0:16 offset1:24
	v_cvt_pk_f16_f32 v1, v48, v49
	v_cvt_pk_f16_f32 v0, v46, v47
	v_cvt_pk_f16_f32 v45, v44, v45
	v_cvt_pk_f16_f32 v44, v42, v43
	ds_write2st64_b64 v100, v[0:1], v[44:45] offset0:32 offset1:40
	v_cvt_pk_f16_f32 v1, v40, v41
	v_cvt_pk_f16_f32 v0, v38, v39
	v_cvt_pk_f16_f32 v37, v36, v37
	v_cvt_pk_f16_f32 v36, v34, v35
	ds_write2st64_b64 v100, v[0:1], v[36:37] offset0:48 offset1:56
	s_add_u32 s0, s22, 0x200
	s_addc_u32 s1, s90, 0
	s_add_u32 s70, s0, 0x20000
	s_addc_u32 s71, s1, 0
	s_add_u32 s72, s0, 0x40000
	s_addc_u32 s73, s1, 0
	s_add_u32 s92, s0, 0x60000
	s_addc_u32 s93, s1, 0
	s_add_u32 s94, s0, 0x80000
	s_addc_u32 s95, s1, 0
	s_add_u32 s96, s0, 0xa0000
	s_addc_u32 s97, s1, 0
	s_add_u32 s98, s0, 0xc0000
	s_addc_u32 s99, s1, 0
	s_add_u32 s80, s0, 0xe0000
	s_addc_u32 s81, s1, 0
	global_load_dwordx4 v[70:73], v201, s[0:1] nt
	global_load_dwordx4 v[42:45], v201, s[70:71] nt
	global_load_dwordx4 v[46:49], v201, s[72:73] nt
	global_load_dwordx4 v[66:69], v201, s[92:93] nt
	global_load_dwordx4 v[62:65], v201, s[94:95] nt
	global_load_dwordx4 v[58:61], v201, s[96:97] nt
	global_load_dwordx4 v[54:57], v201, s[98:99] nt
	global_load_dwordx4 v[50:53], v201, s[80:81] nt
	s_waitcnt vmcnt(8)
	s_waitcnt lgkmcnt(0)
	s_barrier
	ds_read_b128 v[34:37], v131
	ds_read_b128 v[38:41], v131 offset:2048
	ds_read_b128 v[74:77], v131 offset:4096
	ds_read_b128 v[78:81], v131 offset:6144
	ds_read_b128 v[82:85], v129
	ds_read_b128 v[86:89], v129 offset:2048
	s_add_u32 s70, s22, 0x300
	v_add_u32_e32 v95, 0x8000, v94
	v_lshl_add_u64 v[0:1], s[26:27], 0, v[196:197]
	s_addc_u32 s71, s90, 0
	v_readfirstlane_b32 s0, v95
	s_mov_b32 m0, s0
	v_cvt_pk_f16_f32 v33, v32, v33
	global_load_lds_dwordx4 v[0:1], off
	v_cvt_pk_f16_f32 v32, v30, v31
	ds_write_b64 v100, v[32:33] offset:32768
	global_load_dwordx4 v[30:33], v201, s[70:71] nt
	s_setprio 1
	s_waitcnt lgkmcnt(1)
	v_mfma_f32_16x16x32_f16 v[90:93], v[82:85], v[34:37], 0
	v_mfma_f32_16x16x32_f16 v[102:105], v[82:85], v[38:41], 0
	v_mfma_f32_16x16x32_f16 v[106:109], v[82:85], v[74:77], 0
	v_mfma_f32_16x16x32_f16 v[82:85], v[82:85], v[78:81], 0
	v_mfma_f32_16x16x32_f16 v[110:113], v[86:89], v[34:37], 0
	v_mfma_f32_16x16x32_f16 v[114:117], v[86:89], v[38:41], 0
	v_mfma_f32_16x16x32_f16 v[118:121], v[86:89], v[74:77], 0
	v_mfma_f32_16x16x32_f16 v[86:89], v[86:89], v[78:81], 0
	s_setprio 0
	ds_read_b128 v[122:125], v129 offset:4096
	ds_read_b128 v[134:137], v129 offset:6144
	v_add_u32_e32 v96, 0xa000, v94
	v_lshl_add_u64 v[98:99], v[0:1], 0, s[58:59]
	v_readfirstlane_b32 s1, v96
	s_mov_b32 m0, s1
	v_cvt_pk_f16_f32 v29, v28, v29
	global_load_lds_dwordx4 v[98:99], off
	v_cvt_pk_f16_f32 v28, v26, v27
	ds_write_b64 v100, v[28:29] offset:36864
	s_add_u32 s70, s22, 0x20300
	s_addc_u32 s71, s90, 0
	global_load_dwordx4 v[26:29], v201, s[70:71] nt
	s_setprio 1
	s_waitcnt lgkmcnt(1)
	v_mfma_f32_16x16x32_f16 v[138:141], v[122:125], v[34:37], 0
	v_mfma_f32_16x16x32_f16 v[142:145], v[122:125], v[38:41], 0
	v_mfma_f32_16x16x32_f16 v[146:149], v[122:125], v[74:77], 0
	v_mfma_f32_16x16x32_f16 v[122:125], v[122:125], v[78:81], 0
	v_mfma_f32_16x16x32_f16 v[150:153], v[134:137], v[34:37], 0
	v_mfma_f32_16x16x32_f16 v[154:157], v[134:137], v[38:41], 0
	v_mfma_f32_16x16x32_f16 v[158:161], v[134:137], v[74:77], 0
	v_mfma_f32_16x16x32_f16 v[134:137], v[134:137], v[78:81], 0
	s_setprio 0
	ds_read_b128 v[162:165], v129 offset:8192
	ds_read_b128 v[166:169], v129 offset:10240
	v_add_u32_e32 v97, 0xc000, v94
	v_lshl_add_u64 v[98:99], v[0:1], 0, s[60:61]
	v_readfirstlane_b32 s71, v97
	s_mov_b32 m0, s71
	v_cvt_pk_f16_f32 v25, v24, v25
	global_load_lds_dwordx4 v[98:99], off
	v_cvt_pk_f16_f32 v24, v22, v23
	ds_write_b64 v100, v[24:25] offset:40960
	s_add_u32 s72, s22, 0x40300
	s_addc_u32 s73, s90, 0
	global_load_dwordx4 v[22:25], v201, s[72:73] nt
	s_setprio 1
	s_waitcnt lgkmcnt(1)
	v_mfma_f32_16x16x32_f16 v[170:173], v[162:165], v[34:37], 0
	v_mfma_f32_16x16x32_f16 v[174:177], v[162:165], v[38:41], 0
	v_mfma_f32_16x16x32_f16 v[178:181], v[162:165], v[74:77], 0
	v_mfma_f32_16x16x32_f16 v[162:165], v[162:165], v[78:81], 0
	v_mfma_f32_16x16x32_f16 v[182:185], v[166:169], v[34:37], 0
	v_mfma_f32_16x16x32_f16 v[186:189], v[166:169], v[38:41], 0
	v_mfma_f32_16x16x32_f16 v[190:193], v[166:169], v[74:77], 0
	v_mfma_f32_16x16x32_f16 v[166:169], v[166:169], v[78:81], 0
	s_setprio 0
	ds_read_b128 v[202:205], v129 offset:12288
	ds_read_b128 v[206:209], v129 offset:14336
	v_add_u32_e32 v98, 0xe000, v94
	v_lshl_add_u64 v[0:1], v[0:1], 0, s[62:63]
	v_readfirstlane_b32 s72, v98
	s_mov_b32 m0, s72
	s_nop 0
	global_load_lds_dwordx4 v[0:1], off
	v_cvt_pk_f16_f32 v1, v20, v21
	v_cvt_pk_f16_f32 v0, v18, v19
	ds_write_b64 v100, v[0:1] offset:45056
	s_add_u32 s80, s22, 0x60300
	s_addc_u32 s81, s90, 0
	global_load_dwordx4 v[18:21], v201, s[80:81] nt
	s_setprio 1
	s_waitcnt lgkmcnt(1)
	v_mfma_f32_16x16x32_f16 v[210:213], v[202:205], v[34:37], 0
	v_mfma_f32_16x16x32_f16 v[214:217], v[202:205], v[38:41], 0
	v_mfma_f32_16x16x32_f16 v[218:221], v[202:205], v[74:77], 0
	v_mfma_f32_16x16x32_f16 v[202:205], v[202:205], v[78:81], 0
	v_mfma_f32_16x16x32_f16 v[74:77], v[206:209], v[74:77], 0
	v_mfma_f32_16x16x32_f16 v[78:81], v[206:209], v[78:81], 0
	v_mfma_f32_16x16x32_f16 v[222:225], v[206:209], v[34:37], 0
	v_mfma_f32_16x16x32_f16 v[226:229], v[206:209], v[38:41], 0
	s_setprio 0
	ds_read_b128 v[206:209], v128
	ds_read_b128 v[230:233], v128 offset:2048
	ds_read_b128 v[234:237], v128 offset:4096
	ds_read_b128 v[238:241], v128 offset:6144
	ds_read_b128 v[34:37], v130
	ds_read_b128 v[38:41], v130 offset:2048
	v_cvt_pk_f16_f32 v1, v16, v17
	v_cvt_pk_f16_f32 v0, v14, v15
	ds_write_b64 v100, v[0:1] offset:49152
	s_add_u32 s80, s22, 0x80300
	s_addc_u32 s81, s90, 0
	global_load_dwordx4 v[14:17], v201, s[80:81] nt
	s_setprio 1
	s_waitcnt lgkmcnt(1)
	v_mfma_f32_16x16x32_f16 v[90:93], v[34:37], v[206:209], v[90:93]
	v_mfma_f32_16x16x32_f16 v[102:105], v[34:37], v[230:233], v[102:105]
	v_mfma_f32_16x16x32_f16 v[106:109], v[34:37], v[234:237], v[106:109]
	v_mfma_f32_16x16x32_f16 v[82:85], v[34:37], v[238:241], v[82:85]
	v_mfma_f32_16x16x32_f16 v[110:113], v[38:41], v[206:209], v[110:113]
	v_mfma_f32_16x16x32_f16 v[114:117], v[38:41], v[230:233], v[114:117]
	v_mfma_f32_16x16x32_f16 v[118:121], v[38:41], v[234:237], v[118:121]
	v_mfma_f32_16x16x32_f16 v[86:89], v[38:41], v[238:241], v[86:89]
	s_setprio 0
	ds_read_b128 v[34:37], v130 offset:4096
	ds_read_b128 v[38:41], v130 offset:6144
	v_cvt_pk_f16_f32 v1, v12, v13
	v_cvt_pk_f16_f32 v0, v10, v11
	ds_write_b64 v100, v[0:1] offset:53248
	s_add_u32 s80, s22, 0xa0300
	s_addc_u32 s81, s90, 0
	global_load_dwordx4 v[10:13], v201, s[80:81] nt
	s_setprio 1
	s_waitcnt lgkmcnt(1)
	v_mfma_f32_16x16x32_f16 v[146:149], v[34:37], v[234:237], v[146:149]
	v_mfma_f32_16x16x32_f16 v[122:125], v[34:37], v[238:241], v[122:125]
	v_mfma_f32_16x16x32_f16 v[134:137], v[38:41], v[238:241], v[134:137]
	v_mfma_f32_16x16x32_f16 v[138:141], v[34:37], v[206:209], v[138:141]
	v_mfma_f32_16x16x32_f16 v[142:145], v[34:37], v[230:233], v[142:145]
	v_mfma_f32_16x16x32_f16 v[150:153], v[38:41], v[206:209], v[150:153]
	v_mfma_f32_16x16x32_f16 v[154:157], v[38:41], v[230:233], v[154:157]
	v_mfma_f32_16x16x32_f16 v[158:161], v[38:41], v[234:237], v[158:161]
	s_setprio 0
	ds_read_b128 v[38:41], v130 offset:8192
	ds_read_b128 v[242:245], v130 offset:10240
	v_cvt_pk_f16_f32 v1, v8, v9
	v_cvt_pk_f16_f32 v0, v6, v7
	ds_write_b64 v100, v[0:1] offset:57344
	s_add_u32 s80, s22, 0xc0300
	s_addc_u32 s81, s90, 0
	global_load_dwordx4 v[34:37], v201, s[80:81] nt
	s_setprio 1
	s_waitcnt lgkmcnt(1)
	v_mfma_f32_16x16x32_f16 v[6:9], v[38:41], v[206:209], v[170:173]
	v_mfma_f32_16x16x32_f16 v[170:173], v[38:41], v[230:233], v[174:177]
	v_mfma_f32_16x16x32_f16 v[174:177], v[38:41], v[234:237], v[178:181]
	v_mfma_f32_16x16x32_f16 v[162:165], v[38:41], v[238:241], v[162:165]
	v_mfma_f32_16x16x32_f16 v[178:181], v[242:245], v[206:209], v[182:185]
	v_mfma_f32_16x16x32_f16 v[182:185], v[242:245], v[230:233], v[186:189]
	v_mfma_f32_16x16x32_f16 v[186:189], v[242:245], v[234:237], v[190:193]
	v_mfma_f32_16x16x32_f16 v[166:169], v[242:245], v[238:241], v[166:169]
	s_setprio 0
	s_nop 0
	ds_read_b128 v[190:193], v130 offset:12288
	ds_read_b128 v[242:245], v130 offset:14336
	v_cvt_pk_f16_f32 v1, v4, v5
	v_cvt_pk_f16_f32 v0, v2, v3
	ds_write_b64 v100, v[0:1] offset:61440
	s_add_u32 s80, s22, 0xe0300
	s_addc_u32 s81, s90, 0
	global_load_dwordx4 v[38:41], v201, s[80:81] nt
	s_setprio 1
	s_waitcnt lgkmcnt(1)
	v_mfma_f32_16x16x32_f16 v[78:81], v[242:245], v[238:241], v[78:81]
	v_mfma_f32_16x16x32_f16 v[210:213], v[190:193], v[206:209], v[210:213]
	v_mfma_f32_16x16x32_f16 v[214:217], v[190:193], v[230:233], v[214:217]
	v_mfma_f32_16x16x32_f16 v[218:221], v[190:193], v[234:237], v[218:221]
	v_mfma_f32_16x16x32_f16 v[190:193], v[190:193], v[238:241], v[202:205]
	v_mfma_f32_16x16x32_f16 v[202:205], v[242:245], v[206:209], v[222:225]
	v_mfma_f32_16x16x32_f16 v[206:209], v[242:245], v[230:233], v[226:229]
	v_mfma_f32_16x16x32_f16 v[222:225], v[242:245], v[234:237], v[74:77]
	s_setprio 0
	s_waitcnt vmcnt(4)
	s_waitcnt lgkmcnt(0)
	s_barrier
	ds_read_b128 v[226:229], v131 offset:32768
	ds_read_b128 v[230:233], v131 offset:34816
	ds_read_b128 v[234:237], v131 offset:36864
	ds_read_b128 v[238:241], v131 offset:38912
	ds_read_b128 v[74:77], v129 offset:32768
	ds_read_b128 v[242:245], v129 offset:34816
	s_add_u32 s80, s22, 0x400
	s_addc_u32 s81, s90, 0
	v_lshl_add_u64 v[198:199], s[28:29], 0, v[196:197]
	v_readfirstlane_b32 s70, v94
	s_mov_b32 m0, s70
	v_cvt_pk_f16_f32 v1, v72, v73
	global_load_lds_dwordx4 v[198:199], off
	v_cvt_pk_f16_f32 v0, v70, v71
	ds_write_b64 v100, v[0:1]
	global_load_dwordx4 v[0:3], v201, s[80:81] nt
	s_setprio 1
	s_waitcnt lgkmcnt(1)
	v_mfma_f32_16x16x32_f16 v[70:73], v[74:77], v[226:229], v[90:93]
	v_mfma_f32_16x16x32_f16 v[90:93], v[74:77], v[230:233], v[102:105]
	v_mfma_f32_16x16x32_f16 v[104:107], v[74:77], v[234:237], v[106:109]
	v_mfma_f32_16x16x32_f16 v[82:85], v[74:77], v[238:241], v[82:85]
	v_mfma_f32_16x16x32_f16 v[108:111], v[242:245], v[226:229], v[110:113]
	v_mfma_f32_16x16x32_f16 v[112:115], v[242:245], v[230:233], v[114:117]
	v_mfma_f32_16x16x32_f16 v[116:119], v[242:245], v[234:237], v[118:121]
	v_mfma_f32_16x16x32_f16 v[86:89], v[242:245], v[238:241], v[86:89]
	s_setprio 0
	ds_read_b128 v[74:77], v129 offset:36864
	ds_read_b128 v[242:245], v129 offset:38912
	v_add_u32_e32 v99, 0x2000, v94
	v_lshl_add_u64 v[4:5], v[198:199], 0, s[58:59]
	v_readfirstlane_b32 s73, v99
	s_mov_b32 m0, s73
	s_nop 0
	global_load_lds_dwordx4 v[4:5], off
	v_cvt_pk_f16_f32 v5, v44, v45
	v_cvt_pk_f16_f32 v4, v42, v43
	ds_write_b64 v100, v[4:5] offset:4096
	s_add_u32 s80, s22, 0x20400
	s_addc_u32 s81, s90, 0
	global_load_dwordx4 v[42:45], v201, s[80:81] nt
	s_setprio 1
	s_waitcnt lgkmcnt(1)
	v_mfma_f32_16x16x32_f16 v[146:149], v[74:77], v[234:237], v[146:149]
	v_mfma_f32_16x16x32_f16 v[120:123], v[74:77], v[238:241], v[122:125]
	v_mfma_f32_16x16x32_f16 v[124:127], v[242:245], v[226:229], v[150:153]
	v_mfma_f32_16x16x32_f16 v[134:137], v[242:245], v[238:241], v[134:137]
	v_mfma_f32_16x16x32_f16 v[138:141], v[74:77], v[226:229], v[138:141]
	v_mfma_f32_16x16x32_f16 v[142:145], v[74:77], v[230:233], v[142:145]
	v_mfma_f32_16x16x32_f16 v[150:153], v[242:245], v[230:233], v[154:157]
	v_mfma_f32_16x16x32_f16 v[154:157], v[242:245], v[234:237], v[158:161]
	s_setprio 0
	ds_read_b128 v[74:77], v129 offset:40960
	s_nop 0
	ds_read_b128 v[158:161], v129 offset:43008
	v_add_u32_e32 v101, 0x4000, v94
	v_lshl_add_u64 v[4:5], v[198:199], 0, s[60:61]
	v_readfirstlane_b32 s91, v101
	s_mov_b32 m0, s91
	s_nop 0
	global_load_lds_dwordx4 v[4:5], off
	v_cvt_pk_f16_f32 v5, v48, v49
	v_cvt_pk_f16_f32 v4, v46, v47
	ds_write_b64 v100, v[4:5] offset:8192
	s_add_u32 s80, s22, 0x40400
	s_addc_u32 s81, s90, 0
	global_load_dwordx4 v[46:49], v201, s[80:81] nt
	s_setprio 1
	s_waitcnt lgkmcnt(1)
	v_mfma_f32_16x16x32_f16 v[4:7], v[74:77], v[226:229], v[6:9]
	v_mfma_f32_16x16x32_f16 v[170:173], v[74:77], v[230:233], v[170:173]
	v_mfma_f32_16x16x32_f16 v[174:177], v[74:77], v[234:237], v[174:177]
	v_mfma_f32_16x16x32_f16 v[162:165], v[74:77], v[238:241], v[162:165]
	v_mfma_f32_16x16x32_f16 v[178:181], v[158:161], v[226:229], v[178:181]
	v_mfma_f32_16x16x32_f16 v[182:185], v[158:161], v[230:233], v[182:185]
	v_mfma_f32_16x16x32_f16 v[186:189], v[158:161], v[234:237], v[186:189]
	v_mfma_f32_16x16x32_f16 v[158:161], v[158:161], v[238:241], v[166:169]
	s_setprio 0
	s_nop 1
	ds_read_b128 v[166:169], v129 offset:45056
	ds_read_b128 v[242:245], v129 offset:47104
	v_add_u32_e32 v102, 0x6000, v94
	v_lshl_add_u64 v[8:9], v[198:199], 0, s[62:63]
	v_readfirstlane_b32 s92, v102
	s_mov_b32 m0, s92
	s_nop 0
	global_load_lds_dwordx4 v[8:9], off
	v_cvt_pk_f16_f32 v9, v68, v69
	v_cvt_pk_f16_f32 v8, v66, v67
	ds_write_b64 v100, v[8:9] offset:12288
	s_add_u32 s80, s22, 0x60400
	s_addc_u32 s81, s90, 0
	global_load_dwordx4 v[74:77], v201, s[80:81] nt
	s_setprio 1
	s_waitcnt lgkmcnt(1)
	v_mfma_f32_16x16x32_f16 v[66:69], v[166:169], v[226:229], v[210:213]
	v_mfma_f32_16x16x32_f16 v[210:213], v[166:169], v[230:233], v[214:217]
	v_mfma_f32_16x16x32_f16 v[214:217], v[166:169], v[234:237], v[218:221]
	v_mfma_f32_16x16x32_f16 v[166:169], v[166:169], v[238:241], v[190:193]
	v_mfma_f32_16x16x32_f16 v[190:193], v[242:245], v[226:229], v[202:205]
	v_mfma_f32_16x16x32_f16 v[202:205], v[242:245], v[230:233], v[206:209]
	v_mfma_f32_16x16x32_f16 v[206:209], v[242:245], v[234:237], v[222:225]
	v_mfma_f32_16x16x32_f16 v[218:221], v[242:245], v[238:241], v[78:81]
	s_setprio 0
	s_nop 0
	ds_read_b128 v[222:225], v128 offset:32768
	ds_read_b128 v[226:229], v128 offset:34816
	ds_read_b128 v[230:233], v128 offset:36864
	ds_read_b128 v[234:237], v128 offset:38912
	ds_read_b128 v[238:241], v130 offset:32768
	ds_read_b128 v[242:245], v130 offset:34816
	v_cvt_pk_f16_f32 v9, v64, v65
	v_cvt_pk_f16_f32 v8, v62, v63
	ds_write_b64 v100, v[8:9] offset:16384
	s_add_u32 s80, s22, 0x80400
	s_addc_u32 s81, s90, 0
	global_load_dwordx4 v[78:81], v201, s[80:81] nt
	s_setprio 1
	s_waitcnt lgkmcnt(1)
	v_mfma_f32_16x16x32_f16 v[62:65], v[238:241], v[222:225], v[70:73]
	v_mfma_f32_16x16x32_f16 v[70:73], v[238:241], v[226:229], v[90:93]
	v_mfma_f32_16x16x32_f16 v[104:107], v[238:241], v[230:233], v[104:107]
	v_mfma_f32_16x16x32_f16 v[108:111], v[242:245], v[222:225], v[108:111]
	v_mfma_f32_16x16x32_f16 v[112:115], v[242:245], v[226:229], v[112:115]
	v_mfma_f32_16x16x32_f16 v[116:119], v[242:245], v[230:233], v[116:119]
	v_mfma_f32_16x16x32_f16 v[238:241], v[238:241], v[234:237], v[82:85]
	v_mfma_f32_16x16x32_f16 v[242:245], v[242:245], v[234:237], v[86:89]
	s_setprio 0
	s_nop 1
	ds_read_b128 v[86:89], v130 offset:36864
	ds_read_b128 v[90:93], v130 offset:38912
	v_cvt_pk_f16_f32 v9, v60, v61
	v_cvt_pk_f16_f32 v8, v58, v59
	ds_write_b64 v100, v[8:9] offset:20480
	s_add_u32 s80, s22, 0xa0400
	s_addc_u32 s81, s90, 0
	global_load_dwordx4 v[82:85], v201, s[80:81] nt
	s_setprio 1
	s_waitcnt lgkmcnt(1)
	v_mfma_f32_16x16x32_f16 v[58:61], v[86:89], v[222:225], v[138:141]
	v_mfma_f32_16x16x32_f16 v[138:141], v[86:89], v[226:229], v[142:145]
	v_mfma_f32_16x16x32_f16 v[142:145], v[86:89], v[230:233], v[146:149]
	v_mfma_f32_16x16x32_f16 v[120:123], v[86:89], v[234:237], v[120:123]
	v_mfma_f32_16x16x32_f16 v[124:127], v[90:93], v[222:225], v[124:127]
	v_mfma_f32_16x16x32_f16 v[146:149], v[90:93], v[226:229], v[150:153]
	v_mfma_f32_16x16x32_f16 v[134:137], v[90:93], v[234:237], v[134:137]
	v_mfma_f32_16x16x32_f16 v[150:153], v[90:93], v[230:233], v[154:157]
	s_setprio 0
	ds_read_b128 v[90:93], v130 offset:40960
	s_nop 0
	ds_read_b128 v[154:157], v130 offset:43008
	v_cvt_pk_f16_f32 v9, v56, v57
	v_cvt_pk_f16_f32 v8, v54, v55
	ds_write_b64 v100, v[8:9] offset:24576
	s_add_u32 s80, s22, 0xc0400
	s_addc_u32 s81, s90, 0
	global_load_dwordx4 v[86:89], v201, s[80:81] nt
	s_setprio 1
	s_waitcnt lgkmcnt(1)
	v_mfma_f32_16x16x32_f16 v[246:249], v[90:93], v[222:225], v[4:7]
	v_mfma_f32_16x16x32_f16 v[170:173], v[90:93], v[226:229], v[170:173]
	v_mfma_f32_16x16x32_f16 v[174:177], v[90:93], v[230:233], v[174:177]
	v_mfma_f32_16x16x32_f16 v[162:165], v[90:93], v[234:237], v[162:165]
	v_mfma_f32_16x16x32_f16 v[178:181], v[154:157], v[222:225], v[178:181]
	v_mfma_f32_16x16x32_f16 v[182:185], v[154:157], v[226:229], v[182:185]
	v_mfma_f32_16x16x32_f16 v[186:189], v[154:157], v[230:233], v[186:189]
	v_mfma_f32_16x16x32_f16 v[154:157], v[154:157], v[234:237], v[158:161]
	s_setprio 0
	ds_read_b128 v[4:7], v130 offset:45056
	ds_read_b128 v[54:57], v130 offset:47104
	v_cvt_pk_f16_f32 v9, v52, v53
	v_cvt_pk_f16_f32 v8, v50, v51
	ds_write_b64 v100, v[8:9] offset:28672
	s_add_u32 s80, s22, 0xe0400
	s_addc_u32 s81, s90, 0
	global_load_dwordx4 v[90:93], v201, s[80:81] nt
	s_setprio 1
	s_waitcnt lgkmcnt(1)
	v_mfma_f32_16x16x32_f16 v[66:69], v[4:7], v[222:225], v[66:69]
	v_mfma_f32_16x16x32_f16 v[158:161], v[4:7], v[226:229], v[210:213]
	v_mfma_f32_16x16x32_f16 v[210:213], v[4:7], v[230:233], v[214:217]
	v_mfma_f32_16x16x32_f16 v[166:169], v[4:7], v[234:237], v[166:169]
	v_mfma_f32_16x16x32_f16 v[190:193], v[54:57], v[222:225], v[190:193]
	v_mfma_f32_16x16x32_f16 v[202:205], v[54:57], v[226:229], v[202:205]
	v_mfma_f32_16x16x32_f16 v[206:209], v[54:57], v[230:233], v[206:209]
	v_mfma_f32_16x16x32_f16 v[214:217], v[54:57], v[234:237], v[218:221]
	s_setprio 0
	s_waitcnt vmcnt(4)
	s_waitcnt lgkmcnt(0)
	s_barrier
	s_nop 0
	ds_read_b128 v[218:221], v131
	ds_read_b128 v[222:225], v131 offset:2048
	ds_read_b128 v[226:229], v131 offset:4096
	ds_read_b128 v[230:233], v131 offset:6144
	ds_read_b128 v[50:53], v129
	ds_read_b128 v[54:57], v129 offset:2048
	s_add_u32 s80, s22, 0x500
	v_lshl_add_u64 v[8:9], s[30:31], 0, v[196:197]
	s_addc_u32 s81, s90, 0
	s_mov_b32 m0, s0
	v_cvt_pk_f16_f32 v5, v32, v33
	global_load_lds_dwordx4 v[8:9], off
	v_cvt_pk_f16_f32 v4, v30, v31
	ds_write_b64 v100, v[4:5] offset:32768
	global_load_dwordx4 v[4:7], v201, s[80:81] nt
	s_setprio 1
	s_waitcnt lgkmcnt(1)
	v_mfma_f32_16x16x32_f16 v[30:33], v[50:53], v[218:221], v[62:65]
	v_mfma_f32_16x16x32_f16 v[70:73], v[50:53], v[222:225], v[70:73]
	v_mfma_f32_16x16x32_f16 v[104:107], v[50:53], v[226:229], v[104:107]
	v_mfma_f32_16x16x32_f16 v[108:111], v[54:57], v[218:221], v[108:111]
	v_mfma_f32_16x16x32_f16 v[112:115], v[54:57], v[222:225], v[112:115]
	v_mfma_f32_16x16x32_f16 v[116:119], v[54:57], v[226:229], v[116:119]
	v_mfma_f32_16x16x32_f16 v[234:237], v[50:53], v[230:233], v[238:241]
	v_mfma_f32_16x16x32_f16 v[238:241], v[54:57], v[230:233], v[242:245]
	s_setprio 0
	ds_read_b128 v[54:57], v129 offset:4096
	ds_read_b128 v[62:65], v129 offset:6144
	s_mov_b32 m0, s1
	v_lshl_add_u64 v[50:51], v[8:9], 0, s[58:59]
	global_load_lds_dwordx4 v[50:51], off
	v_cvt_pk_f16_f32 v29, v28, v29
	v_cvt_pk_f16_f32 v28, v26, v27
	ds_write_b64 v100, v[28:29] offset:36864
	s_add_u32 s0, s22, 0x20500
	s_addc_u32 s1, s90, 0
	global_load_dwordx4 v[50:53], v201, s[0:1] nt
	s_setprio 1
	s_waitcnt lgkmcnt(1)
	v_mfma_f32_16x16x32_f16 v[26:29], v[54:57], v[218:221], v[58:61]
	v_mfma_f32_16x16x32_f16 v[120:123], v[54:57], v[230:233], v[120:123]
	v_mfma_f32_16x16x32_f16 v[124:127], v[62:65], v[218:221], v[124:127]
	v_mfma_f32_16x16x32_f16 v[146:149], v[62:65], v[222:225], v[146:149]
	v_mfma_f32_16x16x32_f16 v[134:137], v[62:65], v[230:233], v[134:137]
	v_mfma_f32_16x16x32_f16 v[138:141], v[54:57], v[222:225], v[138:141]
	v_mfma_f32_16x16x32_f16 v[142:145], v[54:57], v[226:229], v[142:145]
	v_mfma_f32_16x16x32_f16 v[150:153], v[62:65], v[226:229], v[150:153]
	s_setprio 0
	ds_read_b128 v[58:61], v129 offset:8192
	ds_read_b128 v[62:65], v129 offset:10240
	s_mov_b32 m0, s71
	v_lshl_add_u64 v[54:55], v[8:9], 0, s[60:61]
	global_load_lds_dwordx4 v[54:55], off
	v_cvt_pk_f16_f32 v25, v24, v25
	v_cvt_pk_f16_f32 v24, v22, v23
	ds_write_b64 v100, v[24:25] offset:40960
	s_add_u32 s0, s22, 0x40500
	s_addc_u32 s1, s90, 0
	global_load_dwordx4 v[54:57], v201, s[0:1] nt
	s_setprio 1
	s_waitcnt lgkmcnt(1)
	v_mfma_f32_16x16x32_f16 v[22:25], v[58:61], v[218:221], v[246:249]
	v_mfma_f32_16x16x32_f16 v[170:173], v[58:61], v[222:225], v[170:173]
	v_mfma_f32_16x16x32_f16 v[174:177], v[58:61], v[226:229], v[174:177]
	v_mfma_f32_16x16x32_f16 v[162:165], v[58:61], v[230:233], v[162:165]
	v_mfma_f32_16x16x32_f16 v[178:181], v[62:65], v[218:221], v[178:181]
	v_mfma_f32_16x16x32_f16 v[182:185], v[62:65], v[222:225], v[182:185]
	v_mfma_f32_16x16x32_f16 v[186:189], v[62:65], v[226:229], v[186:189]
	v_mfma_f32_16x16x32_f16 v[154:157], v[62:65], v[230:233], v[154:157]
	s_setprio 0
	ds_read_b128 v[62:65], v129 offset:12288
	ds_read_b128 v[242:245], v129 offset:14336
	s_mov_b32 m0, s72
	v_lshl_add_u64 v[8:9], v[8:9], 0, s[62:63]
	global_load_lds_dwordx4 v[8:9], off
	v_cvt_pk_f16_f32 v9, v20, v21
	v_cvt_pk_f16_f32 v8, v18, v19
	ds_write_b64 v100, v[8:9] offset:45056
	s_add_u32 s0, s22, 0x60500
	s_addc_u32 s1, s90, 0
	global_load_dwordx4 v[58:61], v201, s[0:1] nt
	s_setprio 1
	s_waitcnt lgkmcnt(1)
	v_mfma_f32_16x16x32_f16 v[18:21], v[62:65], v[218:221], v[66:69]
	v_mfma_f32_16x16x32_f16 v[158:161], v[62:65], v[222:225], v[158:161]
	v_mfma_f32_16x16x32_f16 v[210:213], v[62:65], v[226:229], v[210:213]
	v_mfma_f32_16x16x32_f16 v[166:169], v[62:65], v[230:233], v[166:169]
	v_mfma_f32_16x16x32_f16 v[190:193], v[242:245], v[218:221], v[190:193]
	v_mfma_f32_16x16x32_f16 v[202:205], v[242:245], v[222:225], v[202:205]
	v_mfma_f32_16x16x32_f16 v[206:209], v[242:245], v[226:229], v[206:209]
	v_mfma_f32_16x16x32_f16 v[214:217], v[242:245], v[230:233], v[214:217]
	s_setprio 0
	ds_read_b128 v[218:221], v128
	ds_read_b128 v[222:225], v128 offset:2048
	ds_read_b128 v[226:229], v128 offset:4096
	ds_read_b128 v[230:233], v128 offset:6144
	ds_read_b128 v[66:69], v130
	ds_read_b128 v[242:245], v130 offset:2048
	v_cvt_pk_f16_f32 v9, v16, v17
	v_cvt_pk_f16_f32 v8, v14, v15
	ds_write_b64 v100, v[8:9] offset:49152
	s_add_u32 s0, s22, 0x80500
	s_addc_u32 s1, s90, 0
	global_load_dwordx4 v[62:65], v201, s[0:1] nt
	s_setprio 1
	s_waitcnt lgkmcnt(1)
	v_mfma_f32_16x16x32_f16 v[14:17], v[66:69], v[218:221], v[30:33]
	v_mfma_f32_16x16x32_f16 v[30:33], v[66:69], v[222:225], v[70:73]
	v_mfma_f32_16x16x32_f16 v[104:107], v[66:69], v[226:229], v[104:107]
	v_mfma_f32_16x16x32_f16 v[108:111], v[242:245], v[218:221], v[108:111]
	v_mfma_f32_16x16x32_f16 v[112:115], v[242:245], v[222:225], v[112:115]
	v_mfma_f32_16x16x32_f16 v[116:119], v[242:245], v[226:229], v[116:119]
	v_mfma_f32_16x16x32_f16 v[234:237], v[66:69], v[230:233], v[234:237]
	v_mfma_f32_16x16x32_f16 v[238:241], v[242:245], v[230:233], v[238:241]
	s_setprio 0
	ds_read_b128 v[70:73], v130 offset:4096
	ds_read_b128 v[242:245], v130 offset:6144
	v_cvt_pk_f16_f32 v9, v12, v13
	v_cvt_pk_f16_f32 v8, v10, v11
	ds_write_b64 v100, v[8:9] offset:53248
	s_add_u32 s0, s22, 0xa0500
	s_addc_u32 s1, s90, 0
	global_load_dwordx4 v[66:69], v201, s[0:1] nt
	s_setprio 1
	s_waitcnt lgkmcnt(1)
	v_mfma_f32_16x16x32_f16 v[26:29], v[70:73], v[218:221], v[26:29]
	v_mfma_f32_16x16x32_f16 v[120:123], v[70:73], v[230:233], v[120:123]
	v_mfma_f32_16x16x32_f16 v[124:127], v[242:245], v[218:221], v[124:127]
	v_mfma_f32_16x16x32_f16 v[146:149], v[242:245], v[222:225], v[146:149]
	v_mfma_f32_16x16x32_f16 v[134:137], v[242:245], v[230:233], v[134:137]
	v_mfma_f32_16x16x32_f16 v[138:141], v[70:73], v[222:225], v[138:141]
	v_mfma_f32_16x16x32_f16 v[142:145], v[70:73], v[226:229], v[142:145]
	v_mfma_f32_16x16x32_f16 v[150:153], v[242:245], v[226:229], v[150:153]
	s_setprio 0
	ds_read_b128 v[8:11], v130 offset:8192
	ds_read_b128 v[242:245], v130 offset:10240
	v_cvt_pk_f16_f32 v13, v36, v37
	v_cvt_pk_f16_f32 v12, v34, v35
	ds_write_b64 v100, v[12:13] offset:57344
	s_add_u32 s0, s22, 0xc0500
	s_addc_u32 s1, s90, 0
	global_load_dwordx4 v[70:73], v201, s[0:1] nt
	s_setprio 1
	s_waitcnt lgkmcnt(1)
	v_mfma_f32_16x16x32_f16 v[22:25], v[8:11], v[218:221], v[22:25]
	v_mfma_f32_16x16x32_f16 v[170:173], v[8:11], v[222:225], v[170:173]
	v_mfma_f32_16x16x32_f16 v[174:177], v[8:11], v[226:229], v[174:177]
	v_mfma_f32_16x16x32_f16 v[162:165], v[8:11], v[230:233], v[162:165]
	v_mfma_f32_16x16x32_f16 v[178:181], v[242:245], v[218:221], v[178:181]
	v_mfma_f32_16x16x32_f16 v[182:185], v[242:245], v[222:225], v[182:185]
	v_mfma_f32_16x16x32_f16 v[186:189], v[242:245], v[226:229], v[186:189]
	v_mfma_f32_16x16x32_f16 v[154:157], v[242:245], v[230:233], v[154:157]
	s_setprio 0
	ds_read_b128 v[8:11], v130 offset:12288
	ds_read_b128 v[242:245], v130 offset:14336
	v_cvt_pk_f16_f32 v13, v40, v41
	v_cvt_pk_f16_f32 v12, v38, v39
	ds_write_b64 v100, v[12:13] offset:61440
	s_add_u32 s0, s22, 0xe0500
	s_addc_u32 s1, s90, 0
	global_load_dwordx4 v[36:39], v201, s[0:1] nt
	s_setprio 1
	s_waitcnt lgkmcnt(1)
	v_mfma_f32_16x16x32_f16 v[246:249], v[8:11], v[218:221], v[18:21]
	v_mfma_f32_16x16x32_f16 v[158:161], v[8:11], v[222:225], v[158:161]
	v_mfma_f32_16x16x32_f16 v[210:213], v[8:11], v[226:229], v[210:213]
	v_mfma_f32_16x16x32_f16 v[166:169], v[8:11], v[230:233], v[166:169]
	v_mfma_f32_16x16x32_f16 v[190:193], v[242:245], v[218:221], v[190:193]
	v_mfma_f32_16x16x32_f16 v[202:205], v[242:245], v[222:225], v[202:205]
	v_mfma_f32_16x16x32_f16 v[206:209], v[242:245], v[226:229], v[206:209]
	v_mfma_f32_16x16x32_f16 v[214:217], v[242:245], v[230:233], v[214:217]
	s_setprio 0
	s_waitcnt vmcnt(4)
	s_waitcnt lgkmcnt(0)
	s_barrier
	ds_read_b128 v[218:221], v131 offset:32768
	ds_read_b128 v[222:225], v131 offset:34816
	ds_read_b128 v[226:229], v131 offset:36864
	ds_read_b128 v[230:233], v131 offset:38912
	ds_read_b128 v[8:11], v129 offset:32768
	ds_read_b128 v[18:21], v129 offset:34816
	s_add_u32 s0, s22, 0x600
	s_addc_u32 s1, s90, 0
	v_lshl_add_u64 v[34:35], s[34:35], 0, v[196:197]
	s_mov_b32 m0, s70
	v_cvt_pk_f16_f32 v3, v2, v3
	global_load_lds_dwordx4 v[34:35], off
	v_cvt_pk_f16_f32 v2, v0, v1
	ds_write_b64 v100, v[2:3]
	global_load_dwordx4 v[0:3], v201, s[0:1] nt
	s_setprio 1
	s_waitcnt lgkmcnt(1)
	v_mfma_f32_16x16x32_f16 v[30:33], v[8:11], v[222:225], v[30:33]
	v_mfma_f32_16x16x32_f16 v[104:107], v[8:11], v[226:229], v[104:107]
	v_mfma_f32_16x16x32_f16 v[108:111], v[18:21], v[218:221], v[108:111]
	v_mfma_f32_16x16x32_f16 v[112:115], v[18:21], v[222:225], v[112:115]
	v_mfma_f32_16x16x32_f16 v[116:119], v[18:21], v[226:229], v[116:119]
	v_mfma_f32_16x16x32_f16 v[242:245], v[8:11], v[218:221], v[14:17]
	v_mfma_f32_16x16x32_f16 v[234:237], v[8:11], v[230:233], v[234:237]
	v_mfma_f32_16x16x32_f16 v[238:241], v[18:21], v[230:233], v[238:241]
	s_setprio 0
	ds_read_b128 v[12:15], v129 offset:36864
	ds_read_b128 v[16:19], v129 offset:38912
	s_mov_b32 m0, s73
	v_lshl_add_u64 v[8:9], v[34:35], 0, s[58:59]
	global_load_lds_dwordx4 v[8:9], off
	v_cvt_pk_f16_f32 v9, v44, v45
	v_cvt_pk_f16_f32 v8, v42, v43
	ds_write_b64 v100, v[8:9] offset:4096
	s_add_u32 s0, s22, 0x20600
	s_addc_u32 s1, s90, 0
	global_load_dwordx4 v[8:11], v201, s[0:1] nt
	s_setprio 1
	s_waitcnt lgkmcnt(1)
	v_mfma_f32_16x16x32_f16 v[40:43], v[12:15], v[218:221], v[26:29]
	v_mfma_f32_16x16x32_f16 v[120:123], v[12:15], v[230:233], v[120:123]
	v_mfma_f32_16x16x32_f16 v[124:127], v[16:19], v[218:221], v[124:127]
	v_mfma_f32_16x16x32_f16 v[146:149], v[16:19], v[222:225], v[146:149]
	v_mfma_f32_16x16x32_f16 v[134:137], v[16:19], v[230:233], v[134:137]
	v_mfma_f32_16x16x32_f16 v[138:141], v[12:15], v[222:225], v[138:141]
	v_mfma_f32_16x16x32_f16 v[142:145], v[12:15], v[226:229], v[142:145]
	v_mfma_f32_16x16x32_f16 v[150:153], v[16:19], v[226:229], v[150:153]
	s_setprio 0
	ds_read_b128 v[16:19], v129 offset:40960
	ds_read_b128 v[26:29], v129 offset:43008
	s_mov_b32 m0, s91
	v_lshl_add_u64 v[12:13], v[34:35], 0, s[60:61]
	global_load_lds_dwordx4 v[12:13], off
	v_cvt_pk_f16_f32 v13, v48, v49
	v_cvt_pk_f16_f32 v12, v46, v47
	ds_write_b64 v100, v[12:13] offset:8192
	s_add_u32 s0, s22, 0x40600
	s_addc_u32 s1, s90, 0
	global_load_dwordx4 v[12:15], v201, s[0:1] nt
	s_setprio 1
	s_waitcnt lgkmcnt(1)
	v_mfma_f32_16x16x32_f16 v[44:47], v[16:19], v[218:221], v[22:25]
	v_mfma_f32_16x16x32_f16 v[170:173], v[16:19], v[222:225], v[170:173]
	v_mfma_f32_16x16x32_f16 v[174:177], v[16:19], v[226:229], v[174:177]
	v_mfma_f32_16x16x32_f16 v[162:165], v[16:19], v[230:233], v[162:165]
	v_mfma_f32_16x16x32_f16 v[178:181], v[26:29], v[218:221], v[178:181]
	v_mfma_f32_16x16x32_f16 v[182:185], v[26:29], v[222:225], v[182:185]
	v_mfma_f32_16x16x32_f16 v[186:189], v[26:29], v[226:229], v[186:189]
	v_mfma_f32_16x16x32_f16 v[154:157], v[26:29], v[230:233], v[154:157]
	s_setprio 0
	ds_read_b128 v[20:23], v129 offset:45056
	ds_read_b128 v[24:27], v129 offset:47104
	s_mov_b32 m0, s92
	v_lshl_add_u64 v[16:17], v[34:35], 0, s[62:63]
	global_load_lds_dwordx4 v[16:17], off
	v_cvt_pk_f16_f32 v17, v76, v77
	v_cvt_pk_f16_f32 v16, v74, v75
	ds_write_b64 v100, v[16:17] offset:12288
	s_add_u32 s0, s22, 0x60600
	s_addc_u32 s1, s90, 0
	global_load_dwordx4 v[16:19], v201, s[0:1] nt
	s_setprio 1
	s_waitcnt lgkmcnt(1)
	v_mfma_f32_16x16x32_f16 v[74:77], v[20:23], v[218:221], v[246:249]
	v_mfma_f32_16x16x32_f16 v[158:161], v[20:23], v[222:225], v[158:161]
	v_mfma_f32_16x16x32_f16 v[210:213], v[20:23], v[226:229], v[210:213]
	v_mfma_f32_16x16x32_f16 v[166:169], v[20:23], v[230:233], v[166:169]
	v_mfma_f32_16x16x32_f16 v[190:193], v[24:27], v[218:221], v[190:193]
	v_mfma_f32_16x16x32_f16 v[202:205], v[24:27], v[222:225], v[202:205]
	v_mfma_f32_16x16x32_f16 v[206:209], v[24:27], v[226:229], v[206:209]
	v_mfma_f32_16x16x32_f16 v[214:217], v[24:27], v[230:233], v[214:217]
	s_setprio 0
	ds_read_b128 v[218:221], v128 offset:32768
	ds_read_b128 v[222:225], v128 offset:34816
	ds_read_b128 v[226:229], v128 offset:36864
	ds_read_b128 v[230:233], v128 offset:38912
	ds_read_b128 v[24:27], v130 offset:32768
	ds_read_b128 v[246:249], v130 offset:34816
	v_cvt_pk_f16_f32 v21, v80, v81
	v_cvt_pk_f16_f32 v20, v78, v79
	ds_write_b64 v100, v[20:21] offset:16384
	s_add_u32 s0, s22, 0x80600
	s_addc_u32 s1, s90, 0
	global_load_dwordx4 v[20:23], v201, s[0:1] nt
	s_setprio 1
	s_waitcnt lgkmcnt(1)
	v_mfma_f32_16x16x32_f16 v[78:81], v[24:27], v[218:221], v[242:245]
	v_mfma_f32_16x16x32_f16 v[104:107], v[24:27], v[226:229], v[104:107]
	v_mfma_f32_16x16x32_f16 v[108:111], v[246:249], v[218:221], v[108:111]
	v_mfma_f32_16x16x32_f16 v[112:115], v[246:249], v[222:225], v[112:115]
	v_mfma_f32_16x16x32_f16 v[116:119], v[246:249], v[226:229], v[116:119]
	v_mfma_f32_16x16x32_f16 v[242:245], v[24:27], v[222:225], v[30:33]
	v_mfma_f32_16x16x32_f16 v[234:237], v[24:27], v[230:233], v[234:237]
	v_mfma_f32_16x16x32_f16 v[238:241], v[246:249], v[230:233], v[238:241]
	s_setprio 0
	ds_read_b128 v[28:31], v130 offset:36864
	ds_read_b128 v[32:35], v130 offset:38912
	v_cvt_pk_f16_f32 v25, v84, v85
	v_cvt_pk_f16_f32 v24, v82, v83
	ds_write_b64 v100, v[24:25] offset:20480
	s_add_u32 s0, s22, 0xa0600
	s_addc_u32 s1, s90, 0
	global_load_dwordx4 v[24:27], v201, s[0:1] nt
	s_setprio 1
	s_waitcnt lgkmcnt(1)
	v_mfma_f32_16x16x32_f16 v[82:85], v[28:31], v[218:221], v[40:43]
	v_mfma_f32_16x16x32_f16 v[120:123], v[28:31], v[230:233], v[120:123]
	v_mfma_f32_16x16x32_f16 v[124:127], v[32:35], v[218:221], v[124:127]
	v_mfma_f32_16x16x32_f16 v[146:149], v[32:35], v[222:225], v[146:149]
	v_mfma_f32_16x16x32_f16 v[134:137], v[32:35], v[230:233], v[134:137]
	v_mfma_f32_16x16x32_f16 v[138:141], v[28:31], v[222:225], v[138:141]
	v_mfma_f32_16x16x32_f16 v[142:145], v[28:31], v[226:229], v[142:145]
	v_mfma_f32_16x16x32_f16 v[150:153], v[32:35], v[226:229], v[150:153]
	s_setprio 0
	ds_read_b128 v[32:35], v130 offset:40960
	ds_read_b128 v[40:43], v130 offset:43008
	v_cvt_pk_f16_f32 v29, v88, v89
	v_cvt_pk_f16_f32 v28, v86, v87
	ds_write_b64 v100, v[28:29] offset:24576
	s_add_u32 s0, s22, 0xc0600
	s_addc_u32 s1, s90, 0
	global_load_dwordx4 v[28:31], v201, s[0:1] nt
	s_setprio 1
	s_waitcnt lgkmcnt(1)
	v_mfma_f32_16x16x32_f16 v[86:89], v[32:35], v[218:221], v[44:47]
	v_mfma_f32_16x16x32_f16 v[170:173], v[32:35], v[222:225], v[170:173]
	v_mfma_f32_16x16x32_f16 v[174:177], v[32:35], v[226:229], v[174:177]
	v_mfma_f32_16x16x32_f16 v[162:165], v[32:35], v[230:233], v[162:165]
	v_mfma_f32_16x16x32_f16 v[178:181], v[40:43], v[218:221], v[178:181]
	v_mfma_f32_16x16x32_f16 v[182:185], v[40:43], v[222:225], v[182:185]
	v_mfma_f32_16x16x32_f16 v[186:189], v[40:43], v[226:229], v[186:189]
	v_mfma_f32_16x16x32_f16 v[154:157], v[40:43], v[230:233], v[154:157]
	s_setprio 0
	ds_read_b128 v[40:43], v130 offset:45056
	ds_read_b128 v[44:47], v130 offset:47104
	v_cvt_pk_f16_f32 v33, v92, v93
	v_cvt_pk_f16_f32 v32, v90, v91
	ds_write_b64 v100, v[32:33] offset:28672
	s_add_u32 s0, s22, 0xe0600
	s_addc_u32 s1, s90, 0
	global_load_dwordx4 v[32:35], v201, s[0:1] nt
	s_setprio 1
	s_waitcnt lgkmcnt(1)
	v_mfma_f32_16x16x32_f16 v[74:77], v[40:43], v[218:221], v[74:77]
	v_mfma_f32_16x16x32_f16 v[90:93], v[40:43], v[222:225], v[158:161]
	v_mfma_f32_16x16x32_f16 v[158:161], v[40:43], v[226:229], v[210:213]
	v_mfma_f32_16x16x32_f16 v[166:169], v[40:43], v[230:233], v[166:169]
	v_mfma_f32_16x16x32_f16 v[190:193], v[44:47], v[218:221], v[190:193]
	v_mfma_f32_16x16x32_f16 v[202:205], v[44:47], v[222:225], v[202:205]
	v_mfma_f32_16x16x32_f16 v[206:209], v[44:47], v[226:229], v[206:209]
	v_mfma_f32_16x16x32_f16 v[210:213], v[44:47], v[230:233], v[214:217]
	s_setprio 0
	s_waitcnt vmcnt(4)
	s_waitcnt lgkmcnt(0)
	s_barrier
	s_nop 0
	ds_read_b128 v[214:217], v131
	ds_read_b128 v[218:221], v131 offset:2048
	ds_read_b128 v[222:225], v131 offset:4096
	ds_read_b128 v[226:229], v131 offset:6144
	ds_read_b128 v[40:43], v129
	ds_read_b128 v[44:47], v129 offset:2048
	s_add_u32 s70, s22, 0x700
	s_addc_u32 s71, s90, 0
	v_lshl_add_u64 v[198:199], s[36:37], 0, v[196:197]
	v_readfirstlane_b32 s0, v95
	s_mov_b32 m0, s0
	v_cvt_pk_f16_f32 v7, v6, v7
	global_load_lds_dwordx4 v[198:199], off
	v_cvt_pk_f16_f32 v6, v4, v5
	ds_write_b64 v100, v[6:7] offset:32768
	global_load_dwordx4 v[4:7], v201, s[70:71] nt
	s_setprio 1
	s_waitcnt lgkmcnt(1)
	v_mfma_f32_16x16x32_f16 v[78:81], v[40:43], v[214:217], v[78:81]
	v_mfma_f32_16x16x32_f16 v[104:107], v[40:43], v[222:225], v[104:107]
	v_mfma_f32_16x16x32_f16 v[108:111], v[44:47], v[214:217], v[108:111]
	v_mfma_f32_16x16x32_f16 v[112:115], v[44:47], v[218:221], v[112:115]
	v_mfma_f32_16x16x32_f16 v[116:119], v[44:47], v[222:225], v[116:119]
	v_mfma_f32_16x16x32_f16 v[230:233], v[40:43], v[218:221], v[242:245]
	v_mfma_f32_16x16x32_f16 v[234:237], v[40:43], v[226:229], v[234:237]
	v_mfma_f32_16x16x32_f16 v[238:241], v[44:47], v[226:229], v[238:241]
	s_setprio 0
	ds_read_b128 v[44:47], v129 offset:4096
	ds_read_b128 v[242:245], v129 offset:6144
	v_readfirstlane_b32 s72, v96
	v_lshl_add_u64 v[40:41], v[198:199], 0, s[58:59]
	s_mov_b32 m0, s72
	s_nop 0
	global_load_lds_dwordx4 v[40:41], off
	v_cvt_pk_f16_f32 v41, v52, v53
	v_cvt_pk_f16_f32 v40, v50, v51
	ds_write_b64 v100, v[40:41] offset:36864
	s_add_u32 s70, s22, 0x20700
	s_addc_u32 s71, s90, 0
	global_load_dwordx4 v[40:43], v201, s[70:71] nt
	s_setprio 1
	s_waitcnt lgkmcnt(1)
	v_mfma_f32_16x16x32_f16 v[82:85], v[44:47], v[214:217], v[82:85]
	v_mfma_f32_16x16x32_f16 v[120:123], v[44:47], v[226:229], v[120:123]
	v_mfma_f32_16x16x32_f16 v[124:127], v[242:245], v[214:217], v[124:127]
	v_mfma_f32_16x16x32_f16 v[146:149], v[242:245], v[218:221], v[146:149]
	v_mfma_f32_16x16x32_f16 v[134:137], v[242:245], v[226:229], v[134:137]
	v_mfma_f32_16x16x32_f16 v[138:141], v[44:47], v[218:221], v[138:141]
	v_mfma_f32_16x16x32_f16 v[142:145], v[44:47], v[222:225], v[142:145]
	v_mfma_f32_16x16x32_f16 v[150:153], v[242:245], v[222:225], v[150:153]
	s_setprio 0
	ds_read_b128 v[48:51], v129 offset:8192
	ds_read_b128 v[242:245], v129 offset:10240
	v_readfirstlane_b32 s71, v97
	v_lshl_add_u64 v[44:45], v[198:199], 0, s[60:61]
	s_mov_b32 m0, s71
	s_nop 0
	global_load_lds_dwordx4 v[44:45], off
	v_cvt_pk_f16_f32 v45, v56, v57
	v_cvt_pk_f16_f32 v44, v54, v55
	ds_write_b64 v100, v[44:45] offset:40960
	s_add_u32 s80, s22, 0x40700
	s_addc_u32 s81, s90, 0
	global_load_dwordx4 v[44:47], v201, s[80:81] nt
	s_setprio 1
	s_waitcnt lgkmcnt(1)
	v_mfma_f32_16x16x32_f16 v[86:89], v[48:51], v[214:217], v[86:89]
	v_mfma_f32_16x16x32_f16 v[170:173], v[48:51], v[218:221], v[170:173]
	v_mfma_f32_16x16x32_f16 v[174:177], v[48:51], v[222:225], v[174:177]
	v_mfma_f32_16x16x32_f16 v[162:165], v[48:51], v[226:229], v[162:165]
	v_mfma_f32_16x16x32_f16 v[178:181], v[242:245], v[214:217], v[178:181]
	v_mfma_f32_16x16x32_f16 v[182:185], v[242:245], v[218:221], v[182:185]
	v_mfma_f32_16x16x32_f16 v[186:189], v[242:245], v[222:225], v[186:189]
	v_mfma_f32_16x16x32_f16 v[154:157], v[242:245], v[226:229], v[154:157]
	s_setprio 0
	ds_read_b128 v[52:55], v129 offset:12288
	ds_read_b128 v[242:245], v129 offset:14336
	v_readfirstlane_b32 s70, v98
	v_lshl_add_u64 v[48:49], v[198:199], 0, s[62:63]
	s_mov_b32 m0, s70
	s_nop 0
	global_load_lds_dwordx4 v[48:49], off
	v_cvt_pk_f16_f32 v49, v60, v61
	v_cvt_pk_f16_f32 v48, v58, v59
	ds_write_b64 v100, v[48:49] offset:45056
	s_add_u32 s80, s22, 0x60700
	s_addc_u32 s81, s90, 0
	global_load_dwordx4 v[48:51], v201, s[80:81] nt
	s_setprio 1
	s_waitcnt lgkmcnt(1)
	v_mfma_f32_16x16x32_f16 v[74:77], v[52:55], v[214:217], v[74:77]
	v_mfma_f32_16x16x32_f16 v[90:93], v[52:55], v[218:221], v[90:93]
	v_mfma_f32_16x16x32_f16 v[158:161], v[52:55], v[222:225], v[158:161]
	v_mfma_f32_16x16x32_f16 v[166:169], v[52:55], v[226:229], v[166:169]
	v_mfma_f32_16x16x32_f16 v[190:193], v[242:245], v[214:217], v[190:193]
	v_mfma_f32_16x16x32_f16 v[202:205], v[242:245], v[218:221], v[202:205]
	v_mfma_f32_16x16x32_f16 v[206:209], v[242:245], v[222:225], v[206:209]
	v_mfma_f32_16x16x32_f16 v[210:213], v[242:245], v[226:229], v[210:213]
	s_setprio 0
	ds_read_b128 v[214:217], v128
	ds_read_b128 v[218:221], v128 offset:2048
	ds_read_b128 v[222:225], v128 offset:4096
	ds_read_b128 v[226:229], v128 offset:6144
	ds_read_b128 v[56:59], v130
	ds_read_b128 v[242:245], v130 offset:2048
	v_cvt_pk_f16_f32 v53, v64, v65
	v_cvt_pk_f16_f32 v52, v62, v63
	ds_write_b64 v100, v[52:53] offset:49152
	s_add_u32 s80, s22, 0x80700
	s_addc_u32 s81, s90, 0
	global_load_dwordx4 v[52:55], v201, s[80:81] nt
	s_setprio 1
	s_waitcnt lgkmcnt(1)
	v_mfma_f32_16x16x32_f16 v[78:81], v[56:59], v[214:217], v[78:81]
	v_mfma_f32_16x16x32_f16 v[104:107], v[56:59], v[222:225], v[104:107]
	v_mfma_f32_16x16x32_f16 v[108:111], v[242:245], v[214:217], v[108:111]
	v_mfma_f32_16x16x32_f16 v[112:115], v[242:245], v[218:221], v[112:115]
	v_mfma_f32_16x16x32_f16 v[116:119], v[242:245], v[222:225], v[116:119]
	v_mfma_f32_16x16x32_f16 v[230:233], v[56:59], v[218:221], v[230:233]
	v_mfma_f32_16x16x32_f16 v[234:237], v[56:59], v[226:229], v[234:237]
	v_mfma_f32_16x16x32_f16 v[238:241], v[242:245], v[226:229], v[238:241]
	s_setprio 0
	ds_read_b128 v[60:63], v130 offset:4096
	ds_read_b128 v[242:245], v130 offset:6144
	v_cvt_pk_f16_f32 v57, v68, v69
	v_cvt_pk_f16_f32 v56, v66, v67
	ds_write_b64 v100, v[56:57] offset:53248
	s_add_u32 s80, s22, 0xa0700
	s_addc_u32 s81, s90, 0
	global_load_dwordx4 v[56:59], v201, s[80:81] nt
	s_setprio 1
	s_waitcnt lgkmcnt(1)
	v_mfma_f32_16x16x32_f16 v[82:85], v[60:63], v[214:217], v[82:85]
	v_mfma_f32_16x16x32_f16 v[120:123], v[60:63], v[226:229], v[120:123]
	v_mfma_f32_16x16x32_f16 v[124:127], v[242:245], v[214:217], v[124:127]
	v_mfma_f32_16x16x32_f16 v[146:149], v[242:245], v[218:221], v[146:149]
	v_mfma_f32_16x16x32_f16 v[134:137], v[242:245], v[226:229], v[134:137]
	v_mfma_f32_16x16x32_f16 v[138:141], v[60:63], v[218:221], v[138:141]
	v_mfma_f32_16x16x32_f16 v[142:145], v[60:63], v[222:225], v[142:145]
	v_mfma_f32_16x16x32_f16 v[150:153], v[242:245], v[222:225], v[150:153]
	s_setprio 0
	ds_read_b128 v[64:67], v130 offset:8192
	ds_read_b128 v[242:245], v130 offset:10240
	v_cvt_pk_f16_f32 v61, v72, v73
	v_cvt_pk_f16_f32 v60, v70, v71
	ds_write_b64 v100, v[60:61] offset:57344
	s_add_u32 s80, s22, 0xc0700
	s_addc_u32 s81, s90, 0
	global_load_dwordx4 v[60:63], v201, s[80:81] nt
	s_setprio 1
	s_waitcnt lgkmcnt(1)
	v_mfma_f32_16x16x32_f16 v[86:89], v[64:67], v[214:217], v[86:89]
	v_mfma_f32_16x16x32_f16 v[170:173], v[64:67], v[218:221], v[170:173]
	v_mfma_f32_16x16x32_f16 v[174:177], v[64:67], v[222:225], v[174:177]
	v_mfma_f32_16x16x32_f16 v[162:165], v[64:67], v[226:229], v[162:165]
	v_mfma_f32_16x16x32_f16 v[178:181], v[242:245], v[214:217], v[178:181]
	v_mfma_f32_16x16x32_f16 v[182:185], v[242:245], v[218:221], v[182:185]
	v_mfma_f32_16x16x32_f16 v[186:189], v[242:245], v[222:225], v[186:189]
	v_mfma_f32_16x16x32_f16 v[154:157], v[242:245], v[226:229], v[154:157]
	s_setprio 0
	ds_read_b128 v[64:67], v130 offset:12288
	ds_read_b128 v[68:71], v130 offset:14336
	v_cvt_pk_f16_f32 v39, v38, v39
	v_cvt_pk_f16_f32 v38, v36, v37
	ds_write_b64 v100, v[38:39] offset:61440
	s_add_u32 s80, s22, 0xe0700
	s_addc_u32 s81, s90, 0
	global_load_dwordx4 v[36:39], v201, s[80:81] nt
	s_setprio 1
	s_waitcnt lgkmcnt(1)
	v_mfma_f32_16x16x32_f16 v[90:93], v[64:67], v[218:221], v[90:93]
	v_mfma_f32_16x16x32_f16 v[242:245], v[64:67], v[214:217], v[74:77]
	v_mfma_f32_16x16x32_f16 v[158:161], v[64:67], v[222:225], v[158:161]
	v_mfma_f32_16x16x32_f16 v[166:169], v[64:67], v[226:229], v[166:169]
	v_mfma_f32_16x16x32_f16 v[190:193], v[68:71], v[214:217], v[190:193]
	v_mfma_f32_16x16x32_f16 v[202:205], v[68:71], v[218:221], v[202:205]
	v_mfma_f32_16x16x32_f16 v[206:209], v[68:71], v[222:225], v[206:209]
	v_mfma_f32_16x16x32_f16 v[210:213], v[68:71], v[226:229], v[210:213]
	s_setprio 0
	s_waitcnt vmcnt(4)
	s_waitcnt lgkmcnt(0)
	s_barrier
	ds_read_b128 v[214:217], v131 offset:32768
	ds_read_b128 v[218:221], v131 offset:34816
	ds_read_b128 v[222:225], v131 offset:36864
	ds_read_b128 v[226:229], v131 offset:38912
	ds_read_b128 v[64:67], v129 offset:32768
	ds_read_b128 v[68:71], v129 offset:34816
	s_add_u32 s80, s22, 0x800
	s_addc_u32 s81, s90, 0
	v_lshl_add_u64 v[198:199], s[38:39], 0, v[196:197]
	v_readfirstlane_b32 s1, v94
	s_mov_b32 m0, s1
	v_cvt_pk_f16_f32 v3, v2, v3
	global_load_lds_dwordx4 v[198:199], off
	v_cvt_pk_f16_f32 v2, v0, v1
	ds_write_b64 v100, v[2:3]
	global_load_dwordx4 v[0:3], v201, s[80:81] nt
	s_setprio 1
	s_waitcnt lgkmcnt(1)
	v_mfma_f32_16x16x32_f16 v[104:107], v[64:67], v[222:225], v[104:107]
	v_mfma_f32_16x16x32_f16 v[108:111], v[68:71], v[214:217], v[108:111]
	v_mfma_f32_16x16x32_f16 v[112:115], v[68:71], v[218:221], v[112:115]
	v_mfma_f32_16x16x32_f16 v[116:119], v[68:71], v[222:225], v[116:119]
	v_mfma_f32_16x16x32_f16 v[246:249], v[64:67], v[214:217], v[78:81]
	v_mfma_f32_16x16x32_f16 v[230:233], v[64:67], v[218:221], v[230:233]
	v_mfma_f32_16x16x32_f16 v[234:237], v[64:67], v[226:229], v[234:237]
	v_mfma_f32_16x16x32_f16 v[238:241], v[68:71], v[226:229], v[238:241]
	s_setprio 0
	ds_read_b128 v[68:71], v129 offset:36864
	ds_read_b128 v[72:75], v129 offset:38912
	v_readfirstlane_b32 s92, v99
	v_lshl_add_u64 v[64:65], v[198:199], 0, s[58:59]
	s_mov_b32 m0, s92
	v_cvt_pk_f16_f32 v11, v10, v11
	global_load_lds_dwordx4 v[64:65], off
	v_cvt_pk_f16_f32 v10, v8, v9
	ds_write_b64 v100, v[10:11] offset:4096
	s_add_u32 s80, s22, 0x20800
	s_addc_u32 s81, s90, 0
	global_load_dwordx4 v[64:67], v201, s[80:81] nt
	s_setprio 1
	s_waitcnt lgkmcnt(1)
	v_mfma_f32_16x16x32_f16 v[8:11], v[68:71], v[214:217], v[82:85]
	v_mfma_f32_16x16x32_f16 v[120:123], v[68:71], v[226:229], v[120:123]
	v_mfma_f32_16x16x32_f16 v[124:127], v[72:75], v[214:217], v[124:127]
	v_mfma_f32_16x16x32_f16 v[146:149], v[72:75], v[218:221], v[146:149]
	v_mfma_f32_16x16x32_f16 v[134:137], v[72:75], v[226:229], v[134:137]
	v_mfma_f32_16x16x32_f16 v[138:141], v[68:71], v[218:221], v[138:141]
	v_mfma_f32_16x16x32_f16 v[142:145], v[68:71], v[222:225], v[142:145]
	v_mfma_f32_16x16x32_f16 v[150:153], v[72:75], v[222:225], v[150:153]
	s_setprio 0
	ds_read_b128 v[72:75], v129 offset:40960
	ds_read_b128 v[76:79], v129 offset:43008
	v_readfirstlane_b32 s91, v101
	v_lshl_add_u64 v[68:69], v[198:199], 0, s[60:61]
	s_mov_b32 m0, s91
	v_cvt_pk_f16_f32 v15, v14, v15
	global_load_lds_dwordx4 v[68:69], off
	v_cvt_pk_f16_f32 v14, v12, v13
	ds_write_b64 v100, v[14:15] offset:8192
	s_add_u32 s80, s22, 0x40800
	s_addc_u32 s81, s90, 0
	global_load_dwordx4 v[68:71], v201, s[80:81] nt
	s_setprio 1
	s_waitcnt lgkmcnt(1)
	v_mfma_f32_16x16x32_f16 v[12:15], v[72:75], v[214:217], v[86:89]
	v_mfma_f32_16x16x32_f16 v[170:173], v[72:75], v[218:221], v[170:173]
	v_mfma_f32_16x16x32_f16 v[174:177], v[72:75], v[222:225], v[174:177]
	v_mfma_f32_16x16x32_f16 v[162:165], v[72:75], v[226:229], v[162:165]
	v_mfma_f32_16x16x32_f16 v[178:181], v[76:79], v[214:217], v[178:181]
	v_mfma_f32_16x16x32_f16 v[182:185], v[76:79], v[218:221], v[182:185]
	v_mfma_f32_16x16x32_f16 v[186:189], v[76:79], v[222:225], v[186:189]
	v_mfma_f32_16x16x32_f16 v[154:157], v[76:79], v[226:229], v[154:157]
	s_setprio 0
	ds_read_b128 v[76:79], v129 offset:45056
	ds_read_b128 v[80:83], v129 offset:47104
	v_readfirstlane_b32 s73, v102
	v_lshl_add_u64 v[72:73], v[198:199], 0, s[62:63]
	s_mov_b32 m0, s73
	v_cvt_pk_f16_f32 v19, v18, v19
	global_load_lds_dwordx4 v[72:73], off
	v_cvt_pk_f16_f32 v18, v16, v17
	ds_write_b64 v100, v[18:19] offset:12288
	s_add_u32 s80, s22, 0x60800
	s_addc_u32 s81, s90, 0
	global_load_dwordx4 v[72:75], v201, s[80:81] nt
	s_setprio 1
	s_waitcnt lgkmcnt(1)
	v_mfma_f32_16x16x32_f16 v[16:19], v[76:79], v[214:217], v[242:245]
	v_mfma_f32_16x16x32_f16 v[242:245], v[76:79], v[218:221], v[90:93]
	v_mfma_f32_16x16x32_f16 v[158:161], v[76:79], v[222:225], v[158:161]
	v_mfma_f32_16x16x32_f16 v[166:169], v[76:79], v[226:229], v[166:169]
	v_mfma_f32_16x16x32_f16 v[190:193], v[80:83], v[214:217], v[190:193]
	v_mfma_f32_16x16x32_f16 v[202:205], v[80:83], v[218:221], v[202:205]
	v_mfma_f32_16x16x32_f16 v[206:209], v[80:83], v[222:225], v[206:209]
	v_mfma_f32_16x16x32_f16 v[210:213], v[80:83], v[226:229], v[210:213]
	s_setprio 0
	ds_read_b128 v[214:217], v128 offset:32768
	ds_read_b128 v[218:221], v128 offset:34816
	ds_read_b128 v[222:225], v128 offset:36864
	ds_read_b128 v[226:229], v128 offset:38912
	ds_read_b128 v[80:83], v130 offset:32768
	ds_read_b128 v[84:87], v130 offset:34816
	v_cvt_pk_f16_f32 v23, v22, v23
	v_cvt_pk_f16_f32 v22, v20, v21
	ds_write_b64 v100, v[22:23] offset:16384
	s_add_u32 s80, s22, 0x80800
	s_addc_u32 s81, s90, 0
	global_load_dwordx4 v[76:79], v201, s[80:81] nt
	s_setprio 1
	s_waitcnt lgkmcnt(1)
	v_mfma_f32_16x16x32_f16 v[20:23], v[80:83], v[214:217], v[246:249]
	v_mfma_f32_16x16x32_f16 v[104:107], v[80:83], v[222:225], v[104:107]
	v_mfma_f32_16x16x32_f16 v[108:111], v[84:87], v[214:217], v[108:111]
	v_mfma_f32_16x16x32_f16 v[112:115], v[84:87], v[218:221], v[112:115]
	v_mfma_f32_16x16x32_f16 v[116:119], v[84:87], v[222:225], v[116:119]
	v_mfma_f32_16x16x32_f16 v[230:233], v[80:83], v[218:221], v[230:233]
	v_mfma_f32_16x16x32_f16 v[234:237], v[80:83], v[226:229], v[234:237]
	v_mfma_f32_16x16x32_f16 v[238:241], v[84:87], v[226:229], v[238:241]
	s_setprio 0
	ds_read_b128 v[84:87], v130 offset:36864
	ds_read_b128 v[88:91], v130 offset:38912
	v_cvt_pk_f16_f32 v27, v26, v27
	v_cvt_pk_f16_f32 v26, v24, v25
	ds_write_b64 v100, v[26:27] offset:20480
	s_add_u32 s80, s22, 0xa0800
	s_addc_u32 s81, s90, 0
	global_load_dwordx4 v[80:83], v201, s[80:81] nt
	s_setprio 1
	s_waitcnt lgkmcnt(1)
	v_mfma_f32_16x16x32_f16 v[24:27], v[84:87], v[214:217], v[8:11]
	v_mfma_f32_16x16x32_f16 v[120:123], v[84:87], v[226:229], v[120:123]
	v_mfma_f32_16x16x32_f16 v[124:127], v[88:91], v[214:217], v[124:127]
	v_mfma_f32_16x16x32_f16 v[146:149], v[88:91], v[218:221], v[146:149]
	v_mfma_f32_16x16x32_f16 v[134:137], v[88:91], v[226:229], v[134:137]
	v_mfma_f32_16x16x32_f16 v[138:141], v[84:87], v[218:221], v[138:141]
	v_mfma_f32_16x16x32_f16 v[142:145], v[84:87], v[222:225], v[142:145]
	v_mfma_f32_16x16x32_f16 v[150:153], v[88:91], v[222:225], v[150:153]
	s_setprio 0
	ds_read_b128 v[8:11], v130 offset:40960
	ds_read_b128 v[88:91], v130 offset:43008
	v_cvt_pk_f16_f32 v31, v30, v31
	v_cvt_pk_f16_f32 v30, v28, v29
	ds_write_b64 v100, v[30:31] offset:24576
	s_add_u32 s80, s22, 0xc0800
	s_addc_u32 s81, s90, 0
	global_load_dwordx4 v[84:87], v201, s[80:81] nt
	s_setprio 1
	s_waitcnt lgkmcnt(1)
	v_mfma_f32_16x16x32_f16 v[12:15], v[8:11], v[214:217], v[12:15]
	v_mfma_f32_16x16x32_f16 v[28:31], v[8:11], v[218:221], v[170:173]
	v_mfma_f32_16x16x32_f16 v[170:173], v[8:11], v[222:225], v[174:177]
	v_mfma_f32_16x16x32_f16 v[162:165], v[8:11], v[226:229], v[162:165]
	v_mfma_f32_16x16x32_f16 v[174:177], v[88:91], v[214:217], v[178:181]
	v_mfma_f32_16x16x32_f16 v[178:181], v[88:91], v[218:221], v[182:185]
	v_mfma_f32_16x16x32_f16 v[182:185], v[88:91], v[222:225], v[186:189]
	v_mfma_f32_16x16x32_f16 v[154:157], v[88:91], v[226:229], v[154:157]
	s_setprio 0
	ds_read_b128 v[8:11], v130 offset:45056
	ds_read_b128 v[186:189], v130 offset:47104
	v_cvt_pk_f16_f32 v35, v34, v35
	v_cvt_pk_f16_f32 v34, v32, v33
	ds_write_b64 v100, v[34:35] offset:28672
	s_add_u32 s80, s22, 0xe0800
	s_addc_u32 s81, s90, 0
	global_load_dwordx4 v[88:91], v201, s[80:81] nt
	s_setprio 1
	s_waitcnt lgkmcnt(1)
	v_mfma_f32_16x16x32_f16 v[16:19], v[8:11], v[214:217], v[16:19]
	v_mfma_f32_16x16x32_f16 v[32:35], v[8:11], v[218:221], v[242:245]
	v_mfma_f32_16x16x32_f16 v[158:161], v[8:11], v[222:225], v[158:161]
	v_mfma_f32_16x16x32_f16 v[166:169], v[8:11], v[226:229], v[166:169]
	v_mfma_f32_16x16x32_f16 v[190:193], v[186:189], v[214:217], v[190:193]
	v_mfma_f32_16x16x32_f16 v[202:205], v[186:189], v[218:221], v[202:205]
	v_mfma_f32_16x16x32_f16 v[206:209], v[186:189], v[222:225], v[206:209]
	v_mfma_f32_16x16x32_f16 v[186:189], v[186:189], v[226:229], v[210:213]
	s_setprio 0
	s_waitcnt vmcnt(4)
	s_waitcnt lgkmcnt(0)
	s_barrier
	s_nop 0
	ds_read_b128 v[210:213], v131
	ds_read_b128 v[214:217], v131 offset:2048
	ds_read_b128 v[218:221], v131 offset:4096
	ds_read_b128 v[222:225], v131 offset:6144
	ds_read_b128 v[8:11], v129
	ds_read_b128 v[226:229], v129 offset:2048
	s_add_u32 s80, s22, 0x900
	v_lshl_add_u64 v[92:93], s[40:41], 0, v[196:197]
	s_addc_u32 s81, s90, 0
	s_mov_b32 m0, s0
	v_cvt_pk_f16_f32 v7, v6, v7
	global_load_lds_dwordx4 v[92:93], off
	v_cvt_pk_f16_f32 v6, v4, v5
	ds_write_b64 v100, v[6:7] offset:32768
	global_load_dwordx4 v[4:7], v201, s[80:81] nt
	s_setprio 1
	s_waitcnt lgkmcnt(1)
	v_mfma_f32_16x16x32_f16 v[20:23], v[8:11], v[210:213], v[20:23]
	v_mfma_f32_16x16x32_f16 v[104:107], v[8:11], v[218:221], v[104:107]
	v_mfma_f32_16x16x32_f16 v[108:111], v[226:229], v[210:213], v[108:111]
	v_mfma_f32_16x16x32_f16 v[112:115], v[226:229], v[214:217], v[112:115]
	v_mfma_f32_16x16x32_f16 v[116:119], v[226:229], v[218:221], v[116:119]
	v_mfma_f32_16x16x32_f16 v[230:233], v[8:11], v[214:217], v[230:233]
	v_mfma_f32_16x16x32_f16 v[234:237], v[8:11], v[222:225], v[234:237]
	v_mfma_f32_16x16x32_f16 v[226:229], v[226:229], v[222:225], v[238:241]
	s_setprio 0
	s_nop 1
	ds_read_b128 v[238:241], v129 offset:4096
	ds_read_b128 v[242:245], v129 offset:6144
	s_mov_b32 m0, s72
	v_lshl_add_u64 v[8:9], v[92:93], 0, s[58:59]
	global_load_lds_dwordx4 v[8:9], off
	v_cvt_pk_f16_f32 v9, v42, v43
	v_cvt_pk_f16_f32 v8, v40, v41
	ds_write_b64 v100, v[8:9] offset:36864
	s_add_u32 s80, s22, 0x20900
	s_addc_u32 s81, s90, 0
	global_load_dwordx4 v[8:11], v201, s[80:81] nt
	s_setprio 1
	s_waitcnt lgkmcnt(1)
	v_mfma_f32_16x16x32_f16 v[24:27], v[238:241], v[210:213], v[24:27]
	v_mfma_f32_16x16x32_f16 v[120:123], v[238:241], v[222:225], v[120:123]
	v_mfma_f32_16x16x32_f16 v[124:127], v[242:245], v[210:213], v[124:127]
	v_mfma_f32_16x16x32_f16 v[146:149], v[242:245], v[214:217], v[146:149]
	v_mfma_f32_16x16x32_f16 v[134:137], v[242:245], v[222:225], v[134:137]
	v_mfma_f32_16x16x32_f16 v[138:141], v[238:241], v[214:217], v[138:141]
	v_mfma_f32_16x16x32_f16 v[142:145], v[238:241], v[218:221], v[142:145]
	v_mfma_f32_16x16x32_f16 v[150:153], v[242:245], v[218:221], v[150:153]
	s_setprio 0
	ds_read_b128 v[238:241], v129 offset:8192
	ds_read_b128 v[242:245], v129 offset:10240
	s_mov_b32 m0, s71
	v_lshl_add_u64 v[40:41], v[92:93], 0, s[60:61]
	global_load_lds_dwordx4 v[40:41], off
	v_cvt_pk_f16_f32 v41, v46, v47
	v_cvt_pk_f16_f32 v40, v44, v45
	ds_write_b64 v100, v[40:41] offset:40960
	s_add_u32 s80, s22, 0x40900
	s_addc_u32 s81, s90, 0
	global_load_dwordx4 v[40:43], v201, s[80:81] nt
	s_setprio 1
	s_waitcnt lgkmcnt(1)
	v_mfma_f32_16x16x32_f16 v[12:15], v[238:241], v[210:213], v[12:15]
	v_mfma_f32_16x16x32_f16 v[28:31], v[238:241], v[214:217], v[28:31]
	v_mfma_f32_16x16x32_f16 v[170:173], v[238:241], v[218:221], v[170:173]
	v_mfma_f32_16x16x32_f16 v[162:165], v[238:241], v[222:225], v[162:165]
	v_mfma_f32_16x16x32_f16 v[174:177], v[242:245], v[210:213], v[174:177]
	v_mfma_f32_16x16x32_f16 v[178:181], v[242:245], v[214:217], v[178:181]
	v_mfma_f32_16x16x32_f16 v[182:185], v[242:245], v[218:221], v[182:185]
	v_mfma_f32_16x16x32_f16 v[154:157], v[242:245], v[222:225], v[154:157]
	s_setprio 0
	ds_read_b128 v[238:241], v129 offset:12288
	ds_read_b128 v[242:245], v129 offset:14336
	s_mov_b32 m0, s70
	v_lshl_add_u64 v[44:45], v[92:93], 0, s[62:63]
	global_load_lds_dwordx4 v[44:45], off
	v_cvt_pk_f16_f32 v45, v50, v51
	v_cvt_pk_f16_f32 v44, v48, v49
	ds_write_b64 v100, v[44:45] offset:45056
	s_add_u32 s70, s22, 0x60900
	s_addc_u32 s71, s90, 0
	global_load_dwordx4 v[44:47], v201, s[70:71] nt
	s_setprio 1
	s_waitcnt lgkmcnt(1)
	v_mfma_f32_16x16x32_f16 v[16:19], v[238:241], v[210:213], v[16:19]
	v_mfma_f32_16x16x32_f16 v[32:35], v[238:241], v[214:217], v[32:35]
	v_mfma_f32_16x16x32_f16 v[158:161], v[238:241], v[218:221], v[158:161]
	v_mfma_f32_16x16x32_f16 v[166:169], v[238:241], v[222:225], v[166:169]
	v_mfma_f32_16x16x32_f16 v[190:193], v[242:245], v[210:213], v[190:193]
	v_mfma_f32_16x16x32_f16 v[202:205], v[242:245], v[214:217], v[202:205]
	v_mfma_f32_16x16x32_f16 v[206:209], v[242:245], v[218:221], v[206:209]
	v_mfma_f32_16x16x32_f16 v[186:189], v[242:245], v[222:225], v[186:189]
	s_setprio 0
	ds_read_b128 v[210:213], v128
	ds_read_b128 v[214:217], v128 offset:2048
	ds_read_b128 v[218:221], v128 offset:4096
	ds_read_b128 v[222:225], v128 offset:6144
	ds_read_b128 v[238:241], v130
	ds_read_b128 v[242:245], v130 offset:2048
	v_cvt_pk_f16_f32 v49, v54, v55
	v_cvt_pk_f16_f32 v48, v52, v53
	ds_write_b64 v100, v[48:49] offset:49152
	s_add_u32 s70, s22, 0x80900
	s_addc_u32 s71, s90, 0
	global_load_dwordx4 v[48:51], v201, s[70:71] nt
	s_setprio 1
	s_waitcnt lgkmcnt(1)
	v_mfma_f32_16x16x32_f16 v[20:23], v[238:241], v[210:213], v[20:23]
	v_mfma_f32_16x16x32_f16 v[104:107], v[238:241], v[218:221], v[104:107]
	v_mfma_f32_16x16x32_f16 v[108:111], v[242:245], v[210:213], v[108:111]
	v_mfma_f32_16x16x32_f16 v[112:115], v[242:245], v[214:217], v[112:115]
	v_mfma_f32_16x16x32_f16 v[116:119], v[242:245], v[218:221], v[116:119]
	v_mfma_f32_16x16x32_f16 v[230:233], v[238:241], v[214:217], v[230:233]
	v_mfma_f32_16x16x32_f16 v[234:237], v[238:241], v[222:225], v[234:237]
	v_mfma_f32_16x16x32_f16 v[226:229], v[242:245], v[222:225], v[226:229]
	s_setprio 0
	ds_read_b128 v[238:241], v130 offset:4096
	ds_read_b128 v[242:245], v130 offset:6144
	v_cvt_pk_f16_f32 v53, v58, v59
	v_cvt_pk_f16_f32 v52, v56, v57
	ds_write_b64 v100, v[52:53] offset:53248
	s_add_u32 s70, s22, 0xa0900
	s_addc_u32 s71, s90, 0
	global_load_dwordx4 v[52:55], v201, s[70:71] nt
	s_setprio 1
	s_waitcnt lgkmcnt(1)
	v_mfma_f32_16x16x32_f16 v[24:27], v[238:241], v[210:213], v[24:27]
	v_mfma_f32_16x16x32_f16 v[120:123], v[238:241], v[222:225], v[120:123]
	v_mfma_f32_16x16x32_f16 v[124:127], v[242:245], v[210:213], v[124:127]
	v_mfma_f32_16x16x32_f16 v[146:149], v[242:245], v[214:217], v[146:149]
	v_mfma_f32_16x16x32_f16 v[134:137], v[242:245], v[222:225], v[134:137]
	v_mfma_f32_16x16x32_f16 v[138:141], v[238:241], v[214:217], v[138:141]
	v_mfma_f32_16x16x32_f16 v[142:145], v[238:241], v[218:221], v[142:145]
	v_mfma_f32_16x16x32_f16 v[150:153], v[242:245], v[218:221], v[150:153]
	s_setprio 0
	ds_read_b128 v[238:241], v130 offset:8192
	ds_read_b128 v[242:245], v130 offset:10240
	v_cvt_pk_f16_f32 v57, v62, v63
	v_cvt_pk_f16_f32 v56, v60, v61
	ds_write_b64 v100, v[56:57] offset:57344
	s_add_u32 s70, s22, 0xc0900
	s_addc_u32 s71, s90, 0
	global_load_dwordx4 v[56:59], v201, s[70:71] nt
	s_setprio 1
	s_waitcnt lgkmcnt(1)
	v_mfma_f32_16x16x32_f16 v[28:31], v[238:241], v[214:217], v[28:31]
	v_mfma_f32_16x16x32_f16 v[246:249], v[238:241], v[210:213], v[12:15]
	v_mfma_f32_16x16x32_f16 v[170:173], v[238:241], v[218:221], v[170:173]
	v_mfma_f32_16x16x32_f16 v[162:165], v[238:241], v[222:225], v[162:165]
	v_mfma_f32_16x16x32_f16 v[174:177], v[242:245], v[210:213], v[174:177]
	v_mfma_f32_16x16x32_f16 v[178:181], v[242:245], v[214:217], v[178:181]
	v_mfma_f32_16x16x32_f16 v[182:185], v[242:245], v[218:221], v[182:185]
	v_mfma_f32_16x16x32_f16 v[154:157], v[242:245], v[222:225], v[154:157]
	s_setprio 0
	ds_read_b128 v[12:15], v130 offset:12288
	ds_read_b128 v[238:241], v130 offset:14336
	v_cvt_pk_f16_f32 v39, v38, v39
	v_cvt_pk_f16_f32 v38, v36, v37
	ds_write_b64 v100, v[38:39] offset:61440
	s_add_u32 s70, s22, 0xe0900
	s_addc_u32 s71, s90, 0
	global_load_dwordx4 v[60:63], v201, s[70:71] nt
	s_setprio 1
	s_waitcnt lgkmcnt(1)
	v_mfma_f32_16x16x32_f16 v[36:39], v[12:15], v[210:213], v[16:19]
	v_mfma_f32_16x16x32_f16 v[32:35], v[12:15], v[214:217], v[32:35]
	v_mfma_f32_16x16x32_f16 v[158:161], v[12:15], v[218:221], v[158:161]
	v_mfma_f32_16x16x32_f16 v[166:169], v[12:15], v[222:225], v[166:169]
	v_mfma_f32_16x16x32_f16 v[190:193], v[238:241], v[210:213], v[190:193]
	v_mfma_f32_16x16x32_f16 v[202:205], v[238:241], v[214:217], v[202:205]
	v_mfma_f32_16x16x32_f16 v[206:209], v[238:241], v[218:221], v[206:209]
	v_mfma_f32_16x16x32_f16 v[186:189], v[238:241], v[222:225], v[186:189]
	s_setprio 0
	s_waitcnt vmcnt(4)
	s_waitcnt lgkmcnt(0)
	s_barrier
	ds_read_b128 v[210:213], v131 offset:32768
	ds_read_b128 v[214:217], v131 offset:34816
	ds_read_b128 v[218:221], v131 offset:36864
	ds_read_b128 v[222:225], v131 offset:38912
	ds_read_b128 v[12:15], v129 offset:32768
	ds_read_b128 v[16:19], v129 offset:34816
	s_add_u32 s70, s22, 0xa00
	v_lshl_add_u64 v[92:93], s[42:43], 0, v[196:197]
	s_addc_u32 s71, s90, 0
	s_mov_b32 m0, s1
	v_cvt_pk_f16_f32 v3, v2, v3
	global_load_lds_dwordx4 v[92:93], off
	v_cvt_pk_f16_f32 v2, v0, v1
	ds_write_b64 v100, v[2:3]
	global_load_dwordx4 v[0:3], v201, s[70:71] nt
	s_setprio 1
	s_waitcnt lgkmcnt(1)
	v_mfma_f32_16x16x32_f16 v[104:107], v[12:15], v[218:221], v[104:107]
	v_mfma_f32_16x16x32_f16 v[108:111], v[16:19], v[210:213], v[108:111]
	v_mfma_f32_16x16x32_f16 v[112:115], v[16:19], v[214:217], v[112:115]
	v_mfma_f32_16x16x32_f16 v[116:119], v[16:19], v[218:221], v[116:119]
	v_mfma_f32_16x16x32_f16 v[238:241], v[12:15], v[210:213], v[20:23]
	v_mfma_f32_16x16x32_f16 v[230:233], v[12:15], v[214:217], v[230:233]
	v_mfma_f32_16x16x32_f16 v[234:237], v[12:15], v[222:225], v[234:237]
	v_mfma_f32_16x16x32_f16 v[226:229], v[16:19], v[222:225], v[226:229]
	s_setprio 0
	ds_read_b128 v[16:19], v129 offset:36864
	ds_read_b128 v[20:23], v129 offset:38912
	s_mov_b32 m0, s92
	v_lshl_add_u64 v[12:13], v[92:93], 0, s[58:59]
	global_load_lds_dwordx4 v[12:13], off
	v_cvt_pk_f16_f32 v13, v66, v67
	v_cvt_pk_f16_f32 v12, v64, v65
	ds_write_b64 v100, v[12:13] offset:4096
	s_add_u32 s0, s22, 0x20a00
	s_addc_u32 s1, s90, 0
	global_load_dwordx4 v[12:15], v201, s[0:1] nt
	s_setprio 1
	s_waitcnt lgkmcnt(1)
	v_mfma_f32_16x16x32_f16 v[64:67], v[16:19], v[210:213], v[24:27]
	v_mfma_f32_16x16x32_f16 v[120:123], v[16:19], v[222:225], v[120:123]
	v_mfma_f32_16x16x32_f16 v[124:127], v[20:23], v[210:213], v[124:127]
	v_mfma_f32_16x16x32_f16 v[146:149], v[20:23], v[214:217], v[146:149]
	v_mfma_f32_16x16x32_f16 v[134:137], v[20:23], v[222:225], v[134:137]
	v_mfma_f32_16x16x32_f16 v[138:141], v[16:19], v[214:217], v[138:141]
	v_mfma_f32_16x16x32_f16 v[142:145], v[16:19], v[218:221], v[142:145]
	v_mfma_f32_16x16x32_f16 v[150:153], v[20:23], v[218:221], v[150:153]
	s_setprio 0
	ds_read_b128 v[20:23], v129 offset:40960
	ds_read_b128 v[24:27], v129 offset:43008
	s_mov_b32 m0, s91
	v_lshl_add_u64 v[16:17], v[92:93], 0, s[60:61]
	global_load_lds_dwordx4 v[16:17], off
	v_cvt_pk_f16_f32 v17, v70, v71
	v_cvt_pk_f16_f32 v16, v68, v69
	ds_write_b64 v100, v[16:17] offset:8192
	s_add_u32 s0, s22, 0x40a00
	s_addc_u32 s1, s90, 0
	global_load_dwordx4 v[16:19], v201, s[0:1] nt
	s_setprio 1
	s_waitcnt lgkmcnt(1)
	v_mfma_f32_16x16x32_f16 v[68:71], v[20:23], v[210:213], v[246:249]
	v_mfma_f32_16x16x32_f16 v[242:245], v[20:23], v[214:217], v[28:31]
	v_mfma_f32_16x16x32_f16 v[170:173], v[20:23], v[218:221], v[170:173]
	v_mfma_f32_16x16x32_f16 v[162:165], v[20:23], v[222:225], v[162:165]
	v_mfma_f32_16x16x32_f16 v[174:177], v[24:27], v[210:213], v[174:177]
	v_mfma_f32_16x16x32_f16 v[178:181], v[24:27], v[214:217], v[178:181]
	v_mfma_f32_16x16x32_f16 v[182:185], v[24:27], v[218:221], v[182:185]
	v_mfma_f32_16x16x32_f16 v[154:157], v[24:27], v[222:225], v[154:157]
	s_setprio 0
	ds_read_b128 v[24:27], v129 offset:45056
	ds_read_b128 v[28:31], v129 offset:47104
	s_mov_b32 m0, s73
	v_lshl_add_u64 v[20:21], v[92:93], 0, s[62:63]
	global_load_lds_dwordx4 v[20:21], off
	v_cvt_pk_f16_f32 v21, v74, v75
	v_cvt_pk_f16_f32 v20, v72, v73
	ds_write_b64 v100, v[20:21] offset:12288
	s_add_u32 s0, s22, 0x60a00
	s_addc_u32 s1, s90, 0
	global_load_dwordx4 v[20:23], v201, s[0:1] nt
	s_setprio 1
	s_waitcnt lgkmcnt(1)
	v_mfma_f32_16x16x32_f16 v[72:75], v[24:27], v[210:213], v[36:39]
	v_mfma_f32_16x16x32_f16 v[246:249], v[24:27], v[214:217], v[32:35]
	v_mfma_f32_16x16x32_f16 v[158:161], v[24:27], v[218:221], v[158:161]
	v_mfma_f32_16x16x32_f16 v[166:169], v[24:27], v[222:225], v[166:169]
	v_mfma_f32_16x16x32_f16 v[190:193], v[28:31], v[210:213], v[190:193]
	v_mfma_f32_16x16x32_f16 v[202:205], v[28:31], v[214:217], v[202:205]
	v_mfma_f32_16x16x32_f16 v[206:209], v[28:31], v[218:221], v[206:209]
	v_mfma_f32_16x16x32_f16 v[186:189], v[28:31], v[222:225], v[186:189]
	s_setprio 0
	ds_read_b128 v[210:213], v128 offset:32768
	ds_read_b128 v[214:217], v128 offset:34816
	ds_read_b128 v[218:221], v128 offset:36864
	ds_read_b128 v[222:225], v128 offset:38912
	ds_read_b128 v[28:31], v130 offset:32768
	ds_read_b128 v[32:35], v130 offset:34816
	v_cvt_pk_f16_f32 v25, v78, v79
	v_cvt_pk_f16_f32 v24, v76, v77
	ds_write_b64 v100, v[24:25] offset:16384
	s_add_u32 s0, s22, 0x80a00
	s_addc_u32 s1, s90, 0
	global_load_dwordx4 v[24:27], v201, s[0:1] nt
	s_setprio 1
	s_waitcnt lgkmcnt(1)
	v_mfma_f32_16x16x32_f16 v[76:79], v[28:31], v[210:213], v[238:241]
	v_mfma_f32_16x16x32_f16 v[104:107], v[28:31], v[218:221], v[104:107]
	v_mfma_f32_16x16x32_f16 v[108:111], v[32:35], v[210:213], v[108:111]
	v_mfma_f32_16x16x32_f16 v[112:115], v[32:35], v[214:217], v[112:115]
	v_mfma_f32_16x16x32_f16 v[116:119], v[32:35], v[218:221], v[116:119]
	v_mfma_f32_16x16x32_f16 v[230:233], v[28:31], v[214:217], v[230:233]
	v_mfma_f32_16x16x32_f16 v[234:237], v[28:31], v[222:225], v[234:237]
	v_mfma_f32_16x16x32_f16 v[226:229], v[32:35], v[222:225], v[226:229]
	s_setprio 0
	ds_read_b128 v[32:35], v130 offset:36864
	ds_read_b128 v[36:39], v130 offset:38912
	v_cvt_pk_f16_f32 v29, v82, v83
	v_cvt_pk_f16_f32 v28, v80, v81
	ds_write_b64 v100, v[28:29] offset:20480
	s_add_u32 s0, s22, 0xa0a00
	s_addc_u32 s1, s90, 0
	global_load_dwordx4 v[28:31], v201, s[0:1] nt
	s_setprio 1
	s_waitcnt lgkmcnt(1)
	v_mfma_f32_16x16x32_f16 v[80:83], v[32:35], v[210:213], v[64:67]
	v_mfma_f32_16x16x32_f16 v[120:123], v[32:35], v[222:225], v[120:123]
	v_mfma_f32_16x16x32_f16 v[124:127], v[36:39], v[210:213], v[124:127]
	v_mfma_f32_16x16x32_f16 v[146:149], v[36:39], v[214:217], v[146:149]
	v_mfma_f32_16x16x32_f16 v[134:137], v[36:39], v[222:225], v[134:137]
	v_mfma_f32_16x16x32_f16 v[138:141], v[32:35], v[214:217], v[138:141]
	v_mfma_f32_16x16x32_f16 v[142:145], v[32:35], v[218:221], v[142:145]
	v_mfma_f32_16x16x32_f16 v[150:153], v[36:39], v[218:221], v[150:153]
	s_setprio 0
	ds_read_b128 v[36:39], v130 offset:40960
	ds_read_b128 v[64:67], v130 offset:43008
	v_cvt_pk_f16_f32 v33, v86, v87
	v_cvt_pk_f16_f32 v32, v84, v85
	ds_write_b64 v100, v[32:33] offset:24576
	s_add_u32 s0, s22, 0xc0a00
	s_addc_u32 s1, s90, 0
	global_load_dwordx4 v[32:35], v201, s[0:1] nt
	s_setprio 1
	s_waitcnt lgkmcnt(1)
	v_mfma_f32_16x16x32_f16 v[68:71], v[36:39], v[210:213], v[68:71]
	v_mfma_f32_16x16x32_f16 v[84:87], v[36:39], v[214:217], v[242:245]
	v_mfma_f32_16x16x32_f16 v[170:173], v[36:39], v[218:221], v[170:173]
	v_mfma_f32_16x16x32_f16 v[162:165], v[36:39], v[222:225], v[162:165]
	v_mfma_f32_16x16x32_f16 v[174:177], v[64:67], v[210:213], v[174:177]
	v_mfma_f32_16x16x32_f16 v[178:181], v[64:67], v[214:217], v[178:181]
	v_mfma_f32_16x16x32_f16 v[182:185], v[64:67], v[218:221], v[182:185]
	v_mfma_f32_16x16x32_f16 v[154:157], v[64:67], v[222:225], v[154:157]
	s_setprio 0
	ds_read_b128 v[64:67], v130 offset:45056
	ds_read_b128 v[238:241], v130 offset:47104
	v_cvt_pk_f16_f32 v37, v90, v91
	v_cvt_pk_f16_f32 v36, v88, v89
	ds_write_b64 v100, v[36:37] offset:28672
	s_add_u32 s0, s22, 0xe0a00
	s_addc_u32 s1, s90, 0
	global_load_dwordx4 v[36:39], v201, s[0:1] nt
	s_setprio 1
	s_waitcnt lgkmcnt(1)
	v_mfma_f32_16x16x32_f16 v[72:75], v[64:67], v[210:213], v[72:75]
	v_mfma_f32_16x16x32_f16 v[88:91], v[64:67], v[214:217], v[246:249]
	v_mfma_f32_16x16x32_f16 v[158:161], v[64:67], v[218:221], v[158:161]
	v_mfma_f32_16x16x32_f16 v[166:169], v[64:67], v[222:225], v[166:169]
	v_mfma_f32_16x16x32_f16 v[190:193], v[238:241], v[210:213], v[190:193]
	v_mfma_f32_16x16x32_f16 v[202:205], v[238:241], v[214:217], v[202:205]
	v_mfma_f32_16x16x32_f16 v[206:209], v[238:241], v[218:221], v[206:209]
	v_mfma_f32_16x16x32_f16 v[186:189], v[238:241], v[222:225], v[186:189]
	s_setprio 0
	s_waitcnt vmcnt(4)
	s_waitcnt lgkmcnt(0)
	s_barrier
	ds_read_b128 v[210:213], v131
	ds_read_b128 v[214:217], v131 offset:2048
	ds_read_b128 v[218:221], v131 offset:4096
	ds_read_b128 v[222:225], v131 offset:6144
	ds_read_b128 v[64:67], v129
	ds_read_b128 v[238:241], v129 offset:2048
	s_add_u32 s70, s22, 0xb00
	v_lshl_add_u64 v[92:93], s[44:45], 0, v[196:197]
	s_addc_u32 s71, s90, 0
	v_readfirstlane_b32 s0, v95
	s_mov_b32 m0, s0
	v_cvt_pk_f16_f32 v7, v6, v7
	global_load_lds_dwordx4 v[92:93], off
	v_cvt_pk_f16_f32 v6, v4, v5
	ds_write_b64 v100, v[6:7] offset:32768
	global_load_dwordx4 v[4:7], v201, s[70:71] nt
	s_setprio 1
	s_waitcnt lgkmcnt(1)
	v_mfma_f32_16x16x32_f16 v[76:79], v[64:67], v[210:213], v[76:79]
	v_mfma_f32_16x16x32_f16 v[104:107], v[64:67], v[218:221], v[104:107]
	v_mfma_f32_16x16x32_f16 v[108:111], v[238:241], v[210:213], v[108:111]
	v_mfma_f32_16x16x32_f16 v[112:115], v[238:241], v[214:217], v[112:115]
	v_mfma_f32_16x16x32_f16 v[116:119], v[238:241], v[218:221], v[116:119]
	v_mfma_f32_16x16x32_f16 v[230:233], v[64:67], v[214:217], v[230:233]
	v_mfma_f32_16x16x32_f16 v[234:237], v[64:67], v[222:225], v[234:237]
	v_mfma_f32_16x16x32_f16 v[226:229], v[238:241], v[222:225], v[226:229]
	s_setprio 0
	ds_read_b128 v[238:241], v129 offset:4096
	ds_read_b128 v[242:245], v129 offset:6144
	v_readfirstlane_b32 s72, v96
	v_lshl_add_u64 v[64:65], v[92:93], 0, s[58:59]
	s_mov_b32 m0, s72
	v_cvt_pk_f16_f32 v11, v10, v11
	global_load_lds_dwordx4 v[64:65], off
	v_cvt_pk_f16_f32 v10, v8, v9
	ds_write_b64 v100, v[10:11] offset:36864
	s_add_u32 s70, s22, 0x20b00
	s_addc_u32 s71, s90, 0
	global_load_dwordx4 v[64:67], v201, s[70:71] nt
	s_setprio 1
	s_waitcnt lgkmcnt(1)
	v_mfma_f32_16x16x32_f16 v[8:11], v[238:241], v[210:213], v[80:83]
	v_mfma_f32_16x16x32_f16 v[80:83], v[238:241], v[214:217], v[138:141]
	v_mfma_f32_16x16x32_f16 v[138:141], v[238:241], v[218:221], v[142:145]
	v_mfma_f32_16x16x32_f16 v[120:123], v[238:241], v[222:225], v[120:123]
	v_mfma_f32_16x16x32_f16 v[124:127], v[242:245], v[210:213], v[124:127]
	v_mfma_f32_16x16x32_f16 v[142:145], v[242:245], v[214:217], v[146:149]
	v_mfma_f32_16x16x32_f16 v[146:149], v[242:245], v[218:221], v[150:153]
	v_mfma_f32_16x16x32_f16 v[134:137], v[242:245], v[222:225], v[134:137]
	s_setprio 0
	s_nop 0
	ds_read_b128 v[150:153], v129 offset:8192
	ds_read_b128 v[238:241], v129 offset:10240
	v_readfirstlane_b32 s71, v97
	v_lshl_add_u64 v[198:199], v[92:93], 0, s[60:61]
	s_mov_b32 m0, s71
	v_cvt_pk_f16_f32 v43, v42, v43
	global_load_lds_dwordx4 v[198:199], off
	v_cvt_pk_f16_f32 v42, v40, v41
	ds_write_b64 v100, v[42:43] offset:40960
	s_add_u32 s80, s22, 0x40b00
	s_addc_u32 s81, s90, 0
	global_load_dwordx4 v[40:43], v201, s[80:81] nt
	s_setprio 1
	s_waitcnt lgkmcnt(1)
	v_mfma_f32_16x16x32_f16 v[68:71], v[150:153], v[210:213], v[68:71]
	v_mfma_f32_16x16x32_f16 v[84:87], v[150:153], v[214:217], v[84:87]
	v_mfma_f32_16x16x32_f16 v[170:173], v[150:153], v[218:221], v[170:173]
	v_mfma_f32_16x16x32_f16 v[150:153], v[150:153], v[222:225], v[162:165]
	v_mfma_f32_16x16x32_f16 v[162:165], v[238:241], v[210:213], v[174:177]
	v_mfma_f32_16x16x32_f16 v[174:177], v[238:241], v[214:217], v[178:181]
	v_mfma_f32_16x16x32_f16 v[178:181], v[238:241], v[218:221], v[182:185]
	v_mfma_f32_16x16x32_f16 v[154:157], v[238:241], v[222:225], v[154:157]
	s_setprio 0
	s_nop 0
	ds_read_b128 v[182:185], v129 offset:12288
	ds_read_b128 v[238:241], v129 offset:14336
	v_readfirstlane_b32 s70, v98
	v_lshl_add_u64 v[92:93], v[92:93], 0, s[62:63]
	s_mov_b32 m0, s70
	v_cvt_pk_f16_f32 v47, v46, v47
	global_load_lds_dwordx4 v[92:93], off
	v_cvt_pk_f16_f32 v46, v44, v45
	ds_write_b64 v100, v[46:47] offset:45056
	s_add_u32 s80, s22, 0x60b00
	s_addc_u32 s81, s90, 0
	global_load_dwordx4 v[44:47], v201, s[80:81] nt
	s_setprio 1
	s_waitcnt lgkmcnt(1)
	v_mfma_f32_16x16x32_f16 v[72:75], v[182:185], v[210:213], v[72:75]
	v_mfma_f32_16x16x32_f16 v[88:91], v[182:185], v[214:217], v[88:91]
	v_mfma_f32_16x16x32_f16 v[158:161], v[182:185], v[218:221], v[158:161]
	v_mfma_f32_16x16x32_f16 v[166:169], v[182:185], v[222:225], v[166:169]
	v_mfma_f32_16x16x32_f16 v[182:185], v[238:241], v[210:213], v[190:193]
	v_mfma_f32_16x16x32_f16 v[190:193], v[238:241], v[214:217], v[202:205]
	v_mfma_f32_16x16x32_f16 v[202:205], v[238:241], v[218:221], v[206:209]
	v_mfma_f32_16x16x32_f16 v[186:189], v[238:241], v[222:225], v[186:189]
	s_setprio 0
	s_nop 0
	ds_read_b128 v[206:209], v128
	ds_read_b128 v[210:213], v128 offset:2048
	ds_read_b128 v[214:217], v128 offset:4096
	ds_read_b128 v[218:221], v128 offset:6144
	ds_read_b128 v[222:225], v130
	ds_read_b128 v[238:241], v130 offset:2048
	v_cvt_pk_f16_f32 v51, v50, v51
	v_cvt_pk_f16_f32 v50, v48, v49
	ds_write_b64 v100, v[50:51] offset:49152
	s_add_u32 s80, s22, 0x80b00
	s_addc_u32 s81, s90, 0
	global_load_dwordx4 v[48:51], v201, s[80:81] nt
	s_setprio 1
	s_waitcnt lgkmcnt(1)
	v_mfma_f32_16x16x32_f16 v[76:79], v[222:225], v[206:209], v[76:79]
	v_mfma_f32_16x16x32_f16 v[104:107], v[222:225], v[214:217], v[104:107]
	v_mfma_f32_16x16x32_f16 v[108:111], v[238:241], v[206:209], v[108:111]
	v_mfma_f32_16x16x32_f16 v[112:115], v[238:241], v[210:213], v[112:115]
	v_mfma_f32_16x16x32_f16 v[116:119], v[238:241], v[214:217], v[116:119]
	v_mfma_f32_16x16x32_f16 v[230:233], v[222:225], v[210:213], v[230:233]
	v_mfma_f32_16x16x32_f16 v[222:225], v[222:225], v[218:221], v[234:237]
	v_mfma_f32_16x16x32_f16 v[226:229], v[238:241], v[218:221], v[226:229]
	s_setprio 0
	s_nop 0
	ds_read_b128 v[234:237], v130 offset:4096
	ds_read_b128 v[238:241], v130 offset:6144
	v_cvt_pk_f16_f32 v55, v54, v55
	v_cvt_pk_f16_f32 v54, v52, v53
	ds_write_b64 v100, v[54:55] offset:53248
	s_add_u32 s80, s22, 0xa0b00
	s_addc_u32 s81, s90, 0
	global_load_dwordx4 v[52:55], v201, s[80:81] nt
	s_setprio 1
	s_waitcnt lgkmcnt(1)
	v_mfma_f32_16x16x32_f16 v[80:83], v[234:237], v[210:213], v[80:83]
	v_mfma_f32_16x16x32_f16 v[120:123], v[234:237], v[218:221], v[120:123]
	v_mfma_f32_16x16x32_f16 v[124:127], v[238:241], v[206:209], v[124:127]
	v_mfma_f32_16x16x32_f16 v[146:149], v[238:241], v[214:217], v[146:149]
	v_mfma_f32_16x16x32_f16 v[134:137], v[238:241], v[218:221], v[134:137]
	v_mfma_f32_16x16x32_f16 v[242:245], v[234:237], v[206:209], v[8:11]
	v_mfma_f32_16x16x32_f16 v[138:141], v[234:237], v[214:217], v[138:141]
	v_mfma_f32_16x16x32_f16 v[142:145], v[238:241], v[210:213], v[142:145]
	s_setprio 0
	ds_read_b128 v[8:11], v130 offset:8192
	ds_read_b128 v[234:237], v130 offset:10240
	v_cvt_pk_f16_f32 v59, v58, v59
	v_cvt_pk_f16_f32 v58, v56, v57
	ds_write_b64 v100, v[58:59] offset:57344
	s_add_u32 s80, s22, 0xc0b00
	s_addc_u32 s81, s90, 0
	global_load_dwordx4 v[56:59], v201, s[80:81] nt
	s_setprio 1
	s_waitcnt lgkmcnt(1)
	v_mfma_f32_16x16x32_f16 v[84:87], v[8:11], v[210:213], v[84:87]
	v_mfma_f32_16x16x32_f16 v[238:241], v[8:11], v[206:209], v[68:71]
	v_mfma_f32_16x16x32_f16 v[170:173], v[8:11], v[214:217], v[170:173]
	v_mfma_f32_16x16x32_f16 v[150:153], v[8:11], v[218:221], v[150:153]
	v_mfma_f32_16x16x32_f16 v[162:165], v[234:237], v[206:209], v[162:165]
	v_mfma_f32_16x16x32_f16 v[174:177], v[234:237], v[210:213], v[174:177]
	v_mfma_f32_16x16x32_f16 v[178:181], v[234:237], v[214:217], v[178:181]
	v_mfma_f32_16x16x32_f16 v[154:157], v[234:237], v[218:221], v[154:157]
	s_setprio 0
	ds_read_b128 v[8:11], v130 offset:12288
	ds_read_b128 v[68:71], v130 offset:14336
	v_cvt_pk_f16_f32 v63, v62, v63
	v_cvt_pk_f16_f32 v62, v60, v61
	ds_write_b64 v100, v[62:63] offset:61440
	s_add_u32 s80, s22, 0xe0b00
	s_addc_u32 s81, s90, 0
	global_load_dwordx4 v[60:63], v201, s[80:81] nt
	s_setprio 1
	s_waitcnt lgkmcnt(1)
	v_mfma_f32_16x16x32_f16 v[88:91], v[8:11], v[210:213], v[88:91]
	v_mfma_f32_16x16x32_f16 v[234:237], v[8:11], v[206:209], v[72:75]
	v_mfma_f32_16x16x32_f16 v[158:161], v[8:11], v[214:217], v[158:161]
	v_mfma_f32_16x16x32_f16 v[166:169], v[8:11], v[218:221], v[166:169]
	v_mfma_f32_16x16x32_f16 v[182:185], v[68:71], v[206:209], v[182:185]
	v_mfma_f32_16x16x32_f16 v[190:193], v[68:71], v[210:213], v[190:193]
	v_mfma_f32_16x16x32_f16 v[202:205], v[68:71], v[214:217], v[202:205]
	v_mfma_f32_16x16x32_f16 v[186:189], v[68:71], v[218:221], v[186:189]
	s_setprio 0
	s_waitcnt vmcnt(4)
	s_waitcnt lgkmcnt(0)
	s_barrier
	ds_read_b128 v[206:209], v131 offset:32768
	ds_read_b128 v[210:213], v131 offset:34816
	ds_read_b128 v[214:217], v131 offset:36864
	ds_read_b128 v[218:221], v131 offset:38912
	ds_read_b128 v[68:71], v129 offset:32768
	ds_read_b128 v[72:75], v129 offset:34816
	s_add_u32 s80, s22, 0xc00
	v_lshl_add_u64 v[92:93], s[46:47], 0, v[196:197]
	s_addc_u32 s81, s90, 0
	v_readfirstlane_b32 s1, v94
	s_mov_b32 m0, s1
	v_cvt_pk_f16_f32 v3, v2, v3
	global_load_lds_dwordx4 v[92:93], off
	v_cvt_pk_f16_f32 v2, v0, v1
	ds_write_b64 v100, v[2:3]
	global_load_dwordx4 v[8:11], v201, s[80:81] nt
	s_setprio 1
	s_waitcnt lgkmcnt(1)
	v_mfma_f32_16x16x32_f16 v[0:3], v[68:71], v[206:209], v[76:79]
	v_mfma_f32_16x16x32_f16 v[104:107], v[68:71], v[214:217], v[104:107]
	v_mfma_f32_16x16x32_f16 v[108:111], v[72:75], v[206:209], v[108:111]
	v_mfma_f32_16x16x32_f16 v[112:115], v[72:75], v[210:213], v[112:115]
	v_mfma_f32_16x16x32_f16 v[116:119], v[72:75], v[214:217], v[116:119]
	v_mfma_f32_16x16x32_f16 v[230:233], v[68:71], v[210:213], v[230:233]
	v_mfma_f32_16x16x32_f16 v[222:225], v[68:71], v[218:221], v[222:225]
	v_mfma_f32_16x16x32_f16 v[226:229], v[72:75], v[218:221], v[226:229]
	s_setprio 0
	ds_read_b128 v[72:75], v129 offset:36864
	ds_read_b128 v[76:79], v129 offset:38912
	v_readfirstlane_b32 s92, v99
	v_lshl_add_u64 v[68:69], v[92:93], 0, s[58:59]
	s_mov_b32 m0, s92
	v_cvt_pk_f16_f32 v15, v14, v15
	global_load_lds_dwordx4 v[68:69], off
	v_cvt_pk_f16_f32 v14, v12, v13
	ds_write_b64 v100, v[14:15] offset:4096
	s_add_u32 s80, s22, 0x20c00
	s_addc_u32 s81, s90, 0
	global_load_dwordx4 v[68:71], v201, s[80:81] nt
	s_setprio 1
	s_waitcnt lgkmcnt(1)
	v_mfma_f32_16x16x32_f16 v[12:15], v[72:75], v[206:209], v[242:245]
	v_mfma_f32_16x16x32_f16 v[120:123], v[72:75], v[218:221], v[120:123]
	v_mfma_f32_16x16x32_f16 v[124:127], v[76:79], v[206:209], v[124:127]
	v_mfma_f32_16x16x32_f16 v[146:149], v[76:79], v[214:217], v[146:149]
	v_mfma_f32_16x16x32_f16 v[134:137], v[76:79], v[218:221], v[134:137]
	v_mfma_f32_16x16x32_f16 v[242:245], v[72:75], v[210:213], v[80:83]
	v_mfma_f32_16x16x32_f16 v[138:141], v[72:75], v[214:217], v[138:141]
	v_mfma_f32_16x16x32_f16 v[142:145], v[76:79], v[210:213], v[142:145]
	s_setprio 0
	ds_read_b128 v[76:79], v129 offset:40960
	ds_read_b128 v[80:83], v129 offset:43008
	v_readfirstlane_b32 s91, v101
	v_lshl_add_u64 v[72:73], v[92:93], 0, s[60:61]
	s_mov_b32 m0, s91
	v_cvt_pk_f16_f32 v19, v18, v19
	global_load_lds_dwordx4 v[72:73], off
	v_cvt_pk_f16_f32 v18, v16, v17
	ds_write_b64 v100, v[18:19] offset:8192
	s_add_u32 s80, s22, 0x40c00
	s_addc_u32 s81, s90, 0
	global_load_dwordx4 v[72:75], v201, s[80:81] nt
	s_setprio 1
	s_waitcnt lgkmcnt(1)
	v_mfma_f32_16x16x32_f16 v[16:19], v[76:79], v[206:209], v[238:241]
	v_mfma_f32_16x16x32_f16 v[238:241], v[76:79], v[210:213], v[84:87]
	v_mfma_f32_16x16x32_f16 v[170:173], v[76:79], v[214:217], v[170:173]
	v_mfma_f32_16x16x32_f16 v[150:153], v[76:79], v[218:221], v[150:153]
	v_mfma_f32_16x16x32_f16 v[162:165], v[80:83], v[206:209], v[162:165]
	v_mfma_f32_16x16x32_f16 v[174:177], v[80:83], v[210:213], v[174:177]
	v_mfma_f32_16x16x32_f16 v[178:181], v[80:83], v[214:217], v[178:181]
	v_mfma_f32_16x16x32_f16 v[154:157], v[80:83], v[218:221], v[154:157]
	s_setprio 0
	ds_read_b128 v[80:83], v129 offset:45056
	ds_read_b128 v[84:87], v129 offset:47104
	v_readfirstlane_b32 s73, v102
	v_lshl_add_u64 v[76:77], v[92:93], 0, s[62:63]
	s_mov_b32 m0, s73
	v_cvt_pk_f16_f32 v23, v22, v23
	global_load_lds_dwordx4 v[76:77], off
	v_cvt_pk_f16_f32 v22, v20, v21
	ds_write_b64 v100, v[22:23] offset:12288
	s_add_u32 s80, s22, 0x60c00
	s_addc_u32 s81, s90, 0
	global_load_dwordx4 v[76:79], v201, s[80:81] nt
	s_setprio 1
	s_waitcnt lgkmcnt(1)
	v_mfma_f32_16x16x32_f16 v[20:23], v[80:83], v[206:209], v[234:237]
	v_mfma_f32_16x16x32_f16 v[234:237], v[80:83], v[210:213], v[88:91]
	v_mfma_f32_16x16x32_f16 v[158:161], v[80:83], v[214:217], v[158:161]
	v_mfma_f32_16x16x32_f16 v[166:169], v[80:83], v[218:221], v[166:169]
	v_mfma_f32_16x16x32_f16 v[182:185], v[84:87], v[206:209], v[182:185]
	v_mfma_f32_16x16x32_f16 v[190:193], v[84:87], v[210:213], v[190:193]
	v_mfma_f32_16x16x32_f16 v[202:205], v[84:87], v[214:217], v[202:205]
	v_mfma_f32_16x16x32_f16 v[186:189], v[84:87], v[218:221], v[186:189]
	s_setprio 0
	ds_read_b128 v[206:209], v128 offset:32768
	ds_read_b128 v[210:213], v128 offset:34816
	ds_read_b128 v[214:217], v128 offset:36864
	ds_read_b128 v[218:221], v128 offset:38912
	ds_read_b128 v[84:87], v130 offset:32768
	ds_read_b128 v[88:91], v130 offset:34816
	v_cvt_pk_f16_f32 v27, v26, v27
	v_cvt_pk_f16_f32 v26, v24, v25
	ds_write_b64 v100, v[26:27] offset:16384
	s_add_u32 s80, s22, 0x80c00
	s_addc_u32 s81, s90, 0
	global_load_dwordx4 v[80:83], v201, s[80:81] nt
	s_setprio 1
	s_waitcnt lgkmcnt(1)
	v_mfma_f32_16x16x32_f16 v[24:27], v[84:87], v[206:209], v[0:3]
	v_mfma_f32_16x16x32_f16 v[104:107], v[84:87], v[214:217], v[104:107]
	v_mfma_f32_16x16x32_f16 v[108:111], v[88:91], v[206:209], v[108:111]
	v_mfma_f32_16x16x32_f16 v[112:115], v[88:91], v[210:213], v[112:115]
	v_mfma_f32_16x16x32_f16 v[116:119], v[88:91], v[214:217], v[116:119]
	v_mfma_f32_16x16x32_f16 v[230:233], v[84:87], v[210:213], v[230:233]
	v_mfma_f32_16x16x32_f16 v[222:225], v[84:87], v[218:221], v[222:225]
	v_mfma_f32_16x16x32_f16 v[226:229], v[88:91], v[218:221], v[226:229]
	s_setprio 0
	ds_read_b128 v[0:3], v130 offset:36864
	ds_read_b128 v[88:91], v130 offset:38912
	v_cvt_pk_f16_f32 v31, v30, v31
	v_cvt_pk_f16_f32 v30, v28, v29
	ds_write_b64 v100, v[30:31] offset:20480
	s_add_u32 s80, s22, 0xa0c00
	s_addc_u32 s81, s90, 0
	global_load_dwordx4 v[84:87], v201, s[80:81] nt
	s_setprio 1
	s_waitcnt lgkmcnt(1)
	v_mfma_f32_16x16x32_f16 v[12:15], v[0:3], v[206:209], v[12:15]
	v_mfma_f32_16x16x32_f16 v[28:31], v[0:3], v[210:213], v[242:245]
	v_mfma_f32_16x16x32_f16 v[120:123], v[0:3], v[218:221], v[120:123]
	v_mfma_f32_16x16x32_f16 v[124:127], v[88:91], v[206:209], v[124:127]
	v_mfma_f32_16x16x32_f16 v[146:149], v[88:91], v[214:217], v[146:149]
	v_mfma_f32_16x16x32_f16 v[134:137], v[88:91], v[218:221], v[134:137]
	v_mfma_f32_16x16x32_f16 v[138:141], v[0:3], v[214:217], v[138:141]
	v_mfma_f32_16x16x32_f16 v[142:145], v[88:91], v[210:213], v[142:145]
	s_setprio 0
	ds_read_b128 v[0:3], v130 offset:40960
	ds_read_b128 v[242:245], v130 offset:43008
	v_cvt_pk_f16_f32 v35, v34, v35
	v_cvt_pk_f16_f32 v34, v32, v33
	ds_write_b64 v100, v[34:35] offset:24576
	s_add_u32 s80, s22, 0xc0c00
	s_addc_u32 s81, s90, 0
	global_load_dwordx4 v[88:91], v201, s[80:81] nt
	s_setprio 1
	s_waitcnt lgkmcnt(1)
	v_mfma_f32_16x16x32_f16 v[16:19], v[0:3], v[206:209], v[16:19]
	v_mfma_f32_16x16x32_f16 v[32:35], v[0:3], v[210:213], v[238:241]
	v_mfma_f32_16x16x32_f16 v[170:173], v[0:3], v[214:217], v[170:173]
	v_mfma_f32_16x16x32_f16 v[150:153], v[0:3], v[218:221], v[150:153]
	v_mfma_f32_16x16x32_f16 v[162:165], v[242:245], v[206:209], v[162:165]
	v_mfma_f32_16x16x32_f16 v[174:177], v[242:245], v[210:213], v[174:177]
	v_mfma_f32_16x16x32_f16 v[178:181], v[242:245], v[214:217], v[178:181]
	v_mfma_f32_16x16x32_f16 v[154:157], v[242:245], v[218:221], v[154:157]
	s_setprio 0
	ds_read_b128 v[0:3], v130 offset:45056
	ds_read_b128 v[238:241], v130 offset:47104
	v_cvt_pk_f16_f32 v39, v38, v39
	v_cvt_pk_f16_f32 v38, v36, v37
	ds_write_b64 v100, v[38:39] offset:28672
	s_add_u32 s80, s22, 0xe0c00
	s_addc_u32 s81, s90, 0
	global_load_dwordx4 v[36:39], v201, s[80:81] nt
	s_setprio 1
	s_waitcnt lgkmcnt(1)
	v_mfma_f32_16x16x32_f16 v[20:23], v[0:3], v[206:209], v[20:23]
	v_mfma_f32_16x16x32_f16 v[234:237], v[0:3], v[210:213], v[234:237]
	v_mfma_f32_16x16x32_f16 v[158:161], v[0:3], v[214:217], v[158:161]
	v_mfma_f32_16x16x32_f16 v[166:169], v[0:3], v[218:221], v[166:169]
	v_mfma_f32_16x16x32_f16 v[182:185], v[238:241], v[206:209], v[182:185]
	v_mfma_f32_16x16x32_f16 v[190:193], v[238:241], v[210:213], v[190:193]
	v_mfma_f32_16x16x32_f16 v[202:205], v[238:241], v[214:217], v[202:205]
	v_mfma_f32_16x16x32_f16 v[186:189], v[238:241], v[218:221], v[186:189]
	s_setprio 0
	s_waitcnt vmcnt(4)
	s_waitcnt lgkmcnt(0)
	s_barrier
	ds_read_b128 v[206:209], v131
	ds_read_b128 v[210:213], v131 offset:2048
	ds_read_b128 v[214:217], v131 offset:4096
	ds_read_b128 v[218:221], v131 offset:6144
	ds_read_b128 v[238:241], v129
	ds_read_b128 v[242:245], v129 offset:2048
	s_add_u32 s80, s22, 0xd00
	v_lshl_add_u64 v[92:93], s[48:49], 0, v[196:197]
	s_addc_u32 s81, s90, 0
	s_mov_b32 m0, s0
	v_cvt_pk_f16_f32 v1, v6, v7
	global_load_lds_dwordx4 v[92:93], off
	v_cvt_pk_f16_f32 v0, v4, v5
	ds_write_b64 v100, v[0:1] offset:32768
	global_load_dwordx4 v[0:3], v201, s[80:81] nt
	s_setprio 1
	s_waitcnt lgkmcnt(1)
	v_mfma_f32_16x16x32_f16 v[24:27], v[238:241], v[206:209], v[24:27]
	v_mfma_f32_16x16x32_f16 v[104:107], v[238:241], v[214:217], v[104:107]
	v_mfma_f32_16x16x32_f16 v[108:111], v[242:245], v[206:209], v[108:111]
	v_mfma_f32_16x16x32_f16 v[112:115], v[242:245], v[210:213], v[112:115]
	v_mfma_f32_16x16x32_f16 v[116:119], v[242:245], v[214:217], v[116:119]
	v_mfma_f32_16x16x32_f16 v[230:233], v[238:241], v[210:213], v[230:233]
	v_mfma_f32_16x16x32_f16 v[222:225], v[238:241], v[218:221], v[222:225]
	v_mfma_f32_16x16x32_f16 v[226:229], v[242:245], v[218:221], v[226:229]
	s_setprio 0
	ds_read_b128 v[238:241], v129 offset:4096
	ds_read_b128 v[242:245], v129 offset:6144
	s_mov_b32 m0, s72
	v_lshl_add_u64 v[4:5], v[92:93], 0, s[58:59]
	global_load_lds_dwordx4 v[4:5], off
	v_cvt_pk_f16_f32 v5, v66, v67
	v_cvt_pk_f16_f32 v4, v64, v65
	ds_write_b64 v100, v[4:5] offset:36864
	s_add_u32 s80, s22, 0x20d00
	s_addc_u32 s81, s90, 0
	global_load_dwordx4 v[4:7], v201, s[80:81] nt
	s_setprio 1
	s_waitcnt lgkmcnt(1)
	v_mfma_f32_16x16x32_f16 v[64:67], v[238:241], v[206:209], v[12:15]
	v_mfma_f32_16x16x32_f16 v[28:31], v[238:241], v[210:213], v[28:31]
	v_mfma_f32_16x16x32_f16 v[120:123], v[238:241], v[218:221], v[120:123]
	v_mfma_f32_16x16x32_f16 v[124:127], v[242:245], v[206:209], v[124:127]
	v_mfma_f32_16x16x32_f16 v[146:149], v[242:245], v[214:217], v[146:149]
	v_mfma_f32_16x16x32_f16 v[134:137], v[242:245], v[218:221], v[134:137]
	v_mfma_f32_16x16x32_f16 v[138:141], v[238:241], v[214:217], v[138:141]
	v_mfma_f32_16x16x32_f16 v[142:145], v[242:245], v[210:213], v[142:145]
	s_setprio 0
	ds_read_b128 v[238:241], v129 offset:8192
	ds_read_b128 v[242:245], v129 offset:10240
	s_mov_b32 m0, s71
	v_lshl_add_u64 v[12:13], v[92:93], 0, s[60:61]
	global_load_lds_dwordx4 v[12:13], off
	v_cvt_pk_f16_f32 v13, v42, v43
	v_cvt_pk_f16_f32 v12, v40, v41
	ds_write_b64 v100, v[12:13] offset:40960
	s_add_u32 s80, s22, 0x40d00
	s_addc_u32 s81, s90, 0
	global_load_dwordx4 v[12:15], v201, s[80:81] nt
	s_setprio 1
	s_waitcnt lgkmcnt(1)
	v_mfma_f32_16x16x32_f16 v[40:43], v[238:241], v[206:209], v[16:19]
	v_mfma_f32_16x16x32_f16 v[32:35], v[238:241], v[210:213], v[32:35]
	v_mfma_f32_16x16x32_f16 v[170:173], v[238:241], v[214:217], v[170:173]
	v_mfma_f32_16x16x32_f16 v[150:153], v[238:241], v[218:221], v[150:153]
	v_mfma_f32_16x16x32_f16 v[162:165], v[242:245], v[206:209], v[162:165]
	v_mfma_f32_16x16x32_f16 v[174:177], v[242:245], v[210:213], v[174:177]
	v_mfma_f32_16x16x32_f16 v[178:181], v[242:245], v[214:217], v[178:181]
	v_mfma_f32_16x16x32_f16 v[154:157], v[242:245], v[218:221], v[154:157]
	s_setprio 0
	ds_read_b128 v[238:241], v129 offset:12288
	ds_read_b128 v[242:245], v129 offset:14336
	s_mov_b32 m0, s70
	v_lshl_add_u64 v[16:17], v[92:93], 0, s[62:63]
	global_load_lds_dwordx4 v[16:17], off
	v_cvt_pk_f16_f32 v17, v46, v47
	v_cvt_pk_f16_f32 v16, v44, v45
	ds_write_b64 v100, v[16:17] offset:45056
	s_add_u32 s70, s22, 0x60d00
	s_addc_u32 s71, s90, 0
	global_load_dwordx4 v[16:19], v201, s[70:71] nt
	s_setprio 1
	s_waitcnt lgkmcnt(1)
	v_mfma_f32_16x16x32_f16 v[44:47], v[238:241], v[206:209], v[20:23]
	v_mfma_f32_16x16x32_f16 v[234:237], v[238:241], v[210:213], v[234:237]
	v_mfma_f32_16x16x32_f16 v[158:161], v[238:241], v[214:217], v[158:161]
	v_mfma_f32_16x16x32_f16 v[166:169], v[238:241], v[218:221], v[166:169]
	v_mfma_f32_16x16x32_f16 v[182:185], v[242:245], v[206:209], v[182:185]
	v_mfma_f32_16x16x32_f16 v[190:193], v[242:245], v[210:213], v[190:193]
	v_mfma_f32_16x16x32_f16 v[202:205], v[242:245], v[214:217], v[202:205]
	v_mfma_f32_16x16x32_f16 v[186:189], v[242:245], v[218:221], v[186:189]
	s_setprio 0
	ds_read_b128 v[206:209], v128
	ds_read_b128 v[210:213], v128 offset:2048
	ds_read_b128 v[214:217], v128 offset:4096
	ds_read_b128 v[218:221], v128 offset:6144
	ds_read_b128 v[238:241], v130
	ds_read_b128 v[242:245], v130 offset:2048
	v_cvt_pk_f16_f32 v21, v50, v51
	v_cvt_pk_f16_f32 v20, v48, v49
	ds_write_b64 v100, v[20:21] offset:49152
	s_add_u32 s70, s22, 0x80d00
	s_addc_u32 s71, s90, 0
	global_load_dwordx4 v[20:23], v201, s[70:71] nt
	s_setprio 1
	s_waitcnt lgkmcnt(1)
	v_mfma_f32_16x16x32_f16 v[48:51], v[238:241], v[206:209], v[24:27]
	v_mfma_f32_16x16x32_f16 v[104:107], v[238:241], v[214:217], v[104:107]
	v_mfma_f32_16x16x32_f16 v[108:111], v[242:245], v[206:209], v[108:111]
	v_mfma_f32_16x16x32_f16 v[112:115], v[242:245], v[210:213], v[112:115]
	v_mfma_f32_16x16x32_f16 v[116:119], v[242:245], v[214:217], v[116:119]
	v_mfma_f32_16x16x32_f16 v[230:233], v[238:241], v[210:213], v[230:233]
	v_mfma_f32_16x16x32_f16 v[222:225], v[238:241], v[218:221], v[222:225]
	v_mfma_f32_16x16x32_f16 v[226:229], v[242:245], v[218:221], v[226:229]
	s_setprio 0
	ds_read_b128 v[238:241], v130 offset:4096
	ds_read_b128 v[242:245], v130 offset:6144
	v_cvt_pk_f16_f32 v25, v54, v55
	v_cvt_pk_f16_f32 v24, v52, v53
	ds_write_b64 v100, v[24:25] offset:53248
	s_add_u32 s70, s22, 0xa0d00
	s_addc_u32 s71, s90, 0
	global_load_dwordx4 v[24:27], v201, s[70:71] nt
	s_setprio 1
	s_waitcnt lgkmcnt(1)
	v_mfma_f32_16x16x32_f16 v[52:55], v[238:241], v[206:209], v[64:67]
	v_mfma_f32_16x16x32_f16 v[64:67], v[238:241], v[210:213], v[28:31]
	v_mfma_f32_16x16x32_f16 v[120:123], v[238:241], v[218:221], v[120:123]
	v_mfma_f32_16x16x32_f16 v[124:127], v[242:245], v[206:209], v[124:127]
	v_mfma_f32_16x16x32_f16 v[146:149], v[242:245], v[214:217], v[146:149]
	v_mfma_f32_16x16x32_f16 v[134:137], v[242:245], v[218:221], v[134:137]
	v_mfma_f32_16x16x32_f16 v[138:141], v[238:241], v[214:217], v[138:141]
	v_mfma_f32_16x16x32_f16 v[142:145], v[242:245], v[210:213], v[142:145]
	s_setprio 0
	ds_read_b128 v[238:241], v130 offset:8192
	ds_read_b128 v[242:245], v130 offset:10240
	v_cvt_pk_f16_f32 v29, v58, v59
	v_cvt_pk_f16_f32 v28, v56, v57
	ds_write_b64 v100, v[28:29] offset:57344
	s_add_u32 s70, s22, 0xc0d00
	s_addc_u32 s71, s90, 0
	global_load_dwordx4 v[28:31], v201, s[70:71] nt
	s_setprio 1
	s_waitcnt lgkmcnt(1)
	v_mfma_f32_16x16x32_f16 v[56:59], v[238:241], v[206:209], v[40:43]
	v_mfma_f32_16x16x32_f16 v[246:249], v[238:241], v[210:213], v[32:35]
	v_mfma_f32_16x16x32_f16 v[170:173], v[238:241], v[214:217], v[170:173]
	v_mfma_f32_16x16x32_f16 v[150:153], v[238:241], v[218:221], v[150:153]
	v_mfma_f32_16x16x32_f16 v[162:165], v[242:245], v[206:209], v[162:165]
	v_mfma_f32_16x16x32_f16 v[174:177], v[242:245], v[210:213], v[174:177]
	v_mfma_f32_16x16x32_f16 v[178:181], v[242:245], v[214:217], v[178:181]
	v_mfma_f32_16x16x32_f16 v[154:157], v[242:245], v[218:221], v[154:157]
	s_setprio 0
	ds_read_b128 v[40:43], v130 offset:12288
	ds_read_b128 v[238:241], v130 offset:14336
	v_cvt_pk_f16_f32 v33, v62, v63
	v_cvt_pk_f16_f32 v32, v60, v61
	ds_write_b64 v100, v[32:33] offset:61440
	s_add_u32 s70, s22, 0xe0d00
	s_addc_u32 s71, s90, 0
	global_load_dwordx4 v[32:35], v201, s[70:71] nt
	s_setprio 1
	s_waitcnt lgkmcnt(1)
	v_mfma_f32_16x16x32_f16 v[60:63], v[40:43], v[206:209], v[44:47]
	v_mfma_f32_16x16x32_f16 v[234:237], v[40:43], v[210:213], v[234:237]
	v_mfma_f32_16x16x32_f16 v[158:161], v[40:43], v[214:217], v[158:161]
	v_mfma_f32_16x16x32_f16 v[166:169], v[40:43], v[218:221], v[166:169]
	v_mfma_f32_16x16x32_f16 v[182:185], v[238:241], v[206:209], v[182:185]
	v_mfma_f32_16x16x32_f16 v[190:193], v[238:241], v[210:213], v[190:193]
	v_mfma_f32_16x16x32_f16 v[202:205], v[238:241], v[214:217], v[202:205]
	v_mfma_f32_16x16x32_f16 v[186:189], v[238:241], v[218:221], v[186:189]
	s_setprio 0
	s_waitcnt vmcnt(4)
	s_waitcnt lgkmcnt(0)
	s_barrier
	ds_read_b128 v[206:209], v131 offset:32768
	ds_read_b128 v[210:213], v131 offset:34816
	ds_read_b128 v[214:217], v131 offset:36864
	ds_read_b128 v[218:221], v131 offset:38912
	ds_read_b128 v[40:43], v129 offset:32768
	ds_read_b128 v[44:47], v129 offset:34816
	s_add_u32 s70, s22, 0xe00
	v_lshl_add_u64 v[92:93], s[50:51], 0, v[196:197]
	s_addc_u32 s71, s90, 0
	s_mov_b32 m0, s1
	v_cvt_pk_f16_f32 v11, v10, v11
	global_load_lds_dwordx4 v[92:93], off
	v_cvt_pk_f16_f32 v10, v8, v9
	ds_write_b64 v100, v[10:11]
	global_load_dwordx4 v[8:11], v201, s[70:71] nt
	s_setprio 1
	s_waitcnt lgkmcnt(1)
	v_mfma_f32_16x16x32_f16 v[104:107], v[40:43], v[214:217], v[104:107]
	v_mfma_f32_16x16x32_f16 v[108:111], v[44:47], v[206:209], v[108:111]
	v_mfma_f32_16x16x32_f16 v[112:115], v[44:47], v[210:213], v[112:115]
	v_mfma_f32_16x16x32_f16 v[116:119], v[44:47], v[214:217], v[116:119]
	v_mfma_f32_16x16x32_f16 v[238:241], v[40:43], v[206:209], v[48:51]
	v_mfma_f32_16x16x32_f16 v[230:233], v[40:43], v[210:213], v[230:233]
	v_mfma_f32_16x16x32_f16 v[222:225], v[40:43], v[218:221], v[222:225]
	v_mfma_f32_16x16x32_f16 v[226:229], v[44:47], v[218:221], v[226:229]
	s_setprio 0
	ds_read_b128 v[44:47], v129 offset:36864
	ds_read_b128 v[48:51], v129 offset:38912
	s_mov_b32 m0, s92
	v_lshl_add_u64 v[40:41], v[92:93], 0, s[58:59]
	global_load_lds_dwordx4 v[40:41], off
	v_cvt_pk_f16_f32 v41, v70, v71
	v_cvt_pk_f16_f32 v40, v68, v69
	ds_write_b64 v100, v[40:41] offset:4096
	s_add_u32 s0, s22, 0x20e00
	s_addc_u32 s1, s90, 0
	global_load_dwordx4 v[40:43], v201, s[0:1] nt
	s_setprio 1
	s_waitcnt lgkmcnt(1)
	v_mfma_f32_16x16x32_f16 v[68:71], v[44:47], v[206:209], v[52:55]
	v_mfma_f32_16x16x32_f16 v[64:67], v[44:47], v[210:213], v[64:67]
	v_mfma_f32_16x16x32_f16 v[120:123], v[44:47], v[218:221], v[120:123]
	v_mfma_f32_16x16x32_f16 v[124:127], v[48:51], v[206:209], v[124:127]
	v_mfma_f32_16x16x32_f16 v[146:149], v[48:51], v[214:217], v[146:149]
	v_mfma_f32_16x16x32_f16 v[134:137], v[48:51], v[218:221], v[134:137]
	v_mfma_f32_16x16x32_f16 v[138:141], v[44:47], v[214:217], v[138:141]
	v_mfma_f32_16x16x32_f16 v[142:145], v[48:51], v[210:213], v[142:145]
	s_setprio 0
	ds_read_b128 v[48:51], v129 offset:40960
	ds_read_b128 v[52:55], v129 offset:43008
	s_mov_b32 m0, s91
	v_lshl_add_u64 v[44:45], v[92:93], 0, s[60:61]
	global_load_lds_dwordx4 v[44:45], off
	v_cvt_pk_f16_f32 v45, v74, v75
	v_cvt_pk_f16_f32 v44, v72, v73
	ds_write_b64 v100, v[44:45] offset:8192
	s_add_u32 s0, s22, 0x40e00
	s_addc_u32 s1, s90, 0
	global_load_dwordx4 v[44:47], v201, s[0:1] nt
	s_setprio 1
	s_waitcnt lgkmcnt(1)
	v_mfma_f32_16x16x32_f16 v[72:75], v[48:51], v[206:209], v[56:59]
	v_mfma_f32_16x16x32_f16 v[242:245], v[48:51], v[210:213], v[246:249]
	v_mfma_f32_16x16x32_f16 v[170:173], v[48:51], v[214:217], v[170:173]
	v_mfma_f32_16x16x32_f16 v[150:153], v[48:51], v[218:221], v[150:153]
	v_mfma_f32_16x16x32_f16 v[162:165], v[52:55], v[206:209], v[162:165]
	v_mfma_f32_16x16x32_f16 v[174:177], v[52:55], v[210:213], v[174:177]
	v_mfma_f32_16x16x32_f16 v[178:181], v[52:55], v[214:217], v[178:181]
	v_mfma_f32_16x16x32_f16 v[154:157], v[52:55], v[218:221], v[154:157]
	s_setprio 0
	ds_read_b128 v[52:55], v129 offset:45056
	ds_read_b128 v[56:59], v129 offset:47104
	s_mov_b32 m0, s73
	v_lshl_add_u64 v[48:49], v[92:93], 0, s[62:63]
	global_load_lds_dwordx4 v[48:49], off
	v_cvt_pk_f16_f32 v49, v78, v79
	v_cvt_pk_f16_f32 v48, v76, v77
	ds_write_b64 v100, v[48:49] offset:12288
	s_add_u32 s0, s22, 0x60e00
	s_addc_u32 s1, s90, 0
	global_load_dwordx4 v[48:51], v201, s[0:1] nt
	s_setprio 1
	s_waitcnt lgkmcnt(1)
	v_mfma_f32_16x16x32_f16 v[76:79], v[52:55], v[206:209], v[60:63]
	v_mfma_f32_16x16x32_f16 v[234:237], v[52:55], v[210:213], v[234:237]
	v_mfma_f32_16x16x32_f16 v[158:161], v[52:55], v[214:217], v[158:161]
	v_mfma_f32_16x16x32_f16 v[166:169], v[52:55], v[218:221], v[166:169]
	v_mfma_f32_16x16x32_f16 v[182:185], v[56:59], v[206:209], v[182:185]
	v_mfma_f32_16x16x32_f16 v[190:193], v[56:59], v[210:213], v[190:193]
	v_mfma_f32_16x16x32_f16 v[202:205], v[56:59], v[214:217], v[202:205]
	v_mfma_f32_16x16x32_f16 v[186:189], v[56:59], v[218:221], v[186:189]
	s_setprio 0
	ds_read_b128 v[206:209], v128 offset:32768
	ds_read_b128 v[210:213], v128 offset:34816
	ds_read_b128 v[214:217], v128 offset:36864
	ds_read_b128 v[218:221], v128 offset:38912
	ds_read_b128 v[56:59], v130 offset:32768
	ds_read_b128 v[60:63], v130 offset:34816
	v_cvt_pk_f16_f32 v53, v82, v83
	v_cvt_pk_f16_f32 v52, v80, v81
	ds_write_b64 v100, v[52:53] offset:16384
	s_add_u32 s0, s22, 0x80e00
	s_addc_u32 s1, s90, 0
	global_load_dwordx4 v[52:55], v201, s[0:1] nt
	s_setprio 1
	s_waitcnt lgkmcnt(1)
	v_mfma_f32_16x16x32_f16 v[80:83], v[56:59], v[206:209], v[238:241]
	v_mfma_f32_16x16x32_f16 v[104:107], v[56:59], v[214:217], v[104:107]
	v_mfma_f32_16x16x32_f16 v[108:111], v[60:63], v[206:209], v[108:111]
	v_mfma_f32_16x16x32_f16 v[112:115], v[60:63], v[210:213], v[112:115]
	v_mfma_f32_16x16x32_f16 v[116:119], v[60:63], v[214:217], v[116:119]
	v_mfma_f32_16x16x32_f16 v[230:233], v[56:59], v[210:213], v[230:233]
	v_mfma_f32_16x16x32_f16 v[222:225], v[56:59], v[218:221], v[222:225]
	v_mfma_f32_16x16x32_f16 v[226:229], v[60:63], v[218:221], v[226:229]
	s_setprio 0
	ds_read_b128 v[60:63], v130 offset:36864
	ds_read_b128 v[238:241], v130 offset:38912
	v_cvt_pk_f16_f32 v57, v86, v87
	v_cvt_pk_f16_f32 v56, v84, v85
	ds_write_b64 v100, v[56:57] offset:20480
	s_add_u32 s0, s22, 0xa0e00
	s_addc_u32 s1, s90, 0
	global_load_dwordx4 v[56:59], v201, s[0:1] nt
	s_setprio 1
	s_waitcnt lgkmcnt(1)
	v_mfma_f32_16x16x32_f16 v[68:71], v[60:63], v[206:209], v[68:71]
	v_mfma_f32_16x16x32_f16 v[64:67], v[60:63], v[210:213], v[64:67]
	v_mfma_f32_16x16x32_f16 v[84:87], v[60:63], v[214:217], v[138:141]
	v_mfma_f32_16x16x32_f16 v[120:123], v[60:63], v[218:221], v[120:123]
	v_mfma_f32_16x16x32_f16 v[124:127], v[238:241], v[206:209], v[124:127]
	v_mfma_f32_16x16x32_f16 v[134:137], v[238:241], v[218:221], v[134:137]
	v_mfma_f32_16x16x32_f16 v[138:141], v[238:241], v[210:213], v[142:145]
	v_mfma_f32_16x16x32_f16 v[142:145], v[238:241], v[214:217], v[146:149]
	s_setprio 0
	s_nop 1
	ds_read_b128 v[146:149], v130 offset:40960
	ds_read_b128 v[238:241], v130 offset:43008
	v_cvt_pk_f16_f32 v61, v90, v91
	v_cvt_pk_f16_f32 v60, v88, v89
	ds_write_b64 v100, v[60:61] offset:24576
	s_add_u32 s0, s22, 0xc0e00
	s_addc_u32 s1, s90, 0
	global_load_dwordx4 v[60:63], v201, s[0:1] nt
	s_setprio 1
	s_waitcnt lgkmcnt(1)
	v_mfma_f32_16x16x32_f16 v[72:75], v[146:149], v[206:209], v[72:75]
	v_mfma_f32_16x16x32_f16 v[88:91], v[146:149], v[210:213], v[242:245]
	v_mfma_f32_16x16x32_f16 v[170:173], v[146:149], v[214:217], v[170:173]
	v_mfma_f32_16x16x32_f16 v[146:149], v[146:149], v[218:221], v[150:153]
	v_mfma_f32_16x16x32_f16 v[150:153], v[238:241], v[206:209], v[162:165]
	v_mfma_f32_16x16x32_f16 v[162:165], v[238:241], v[210:213], v[174:177]
	v_mfma_f32_16x16x32_f16 v[174:177], v[238:241], v[214:217], v[178:181]
	v_mfma_f32_16x16x32_f16 v[154:157], v[238:241], v[218:221], v[154:157]
	s_setprio 0
	s_nop 0
	ds_read_b128 v[178:181], v130 offset:45056
	ds_read_b128 v[238:241], v130 offset:47104
	v_cvt_pk_f16_f32 v39, v38, v39
	v_cvt_pk_f16_f32 v38, v36, v37
	ds_write_b64 v100, v[38:39] offset:28672
	s_add_u32 s0, s22, 0xe0e00
	s_addc_u32 s1, s90, 0
	global_load_dwordx4 v[36:39], v201, s[0:1] nt
	s_setprio 1
	s_waitcnt lgkmcnt(1)
	v_mfma_f32_16x16x32_f16 v[76:79], v[178:181], v[206:209], v[76:79]
	v_mfma_f32_16x16x32_f16 v[234:237], v[178:181], v[210:213], v[234:237]
	v_mfma_f32_16x16x32_f16 v[158:161], v[178:181], v[214:217], v[158:161]
	v_mfma_f32_16x16x32_f16 v[166:169], v[178:181], v[218:221], v[166:169]
	v_mfma_f32_16x16x32_f16 v[178:181], v[238:241], v[206:209], v[182:185]
	v_mfma_f32_16x16x32_f16 v[182:185], v[238:241], v[210:213], v[190:193]
	v_mfma_f32_16x16x32_f16 v[190:193], v[238:241], v[214:217], v[202:205]
	v_mfma_f32_16x16x32_f16 v[186:189], v[238:241], v[218:221], v[186:189]
	s_setprio 0
	s_waitcnt vmcnt(4)
	s_waitcnt lgkmcnt(0)
	s_barrier
	ds_read_b128 v[202:205], v131
	ds_read_b128 v[206:209], v131 offset:2048
	ds_read_b128 v[210:213], v131 offset:4096
	ds_read_b128 v[214:217], v131 offset:6144
	ds_read_b128 v[218:221], v129
	ds_read_b128 v[238:241], v129 offset:2048
	s_add_u32 s70, s22, 0xf00
	v_lshl_add_u64 v[92:93], s[52:53], 0, v[196:197]
	s_addc_u32 s71, s90, 0
	v_readfirstlane_b32 s0, v95
	s_mov_b32 m0, s0
	v_cvt_pk_f16_f32 v3, v2, v3
	global_load_lds_dwordx4 v[92:93], off
	v_cvt_pk_f16_f32 v2, v0, v1
	ds_write_b64 v100, v[2:3] offset:32768
	global_load_dwordx4 v[0:3], v201, s[70:71] nt
	s_setprio 1
	s_waitcnt lgkmcnt(1)
	v_mfma_f32_16x16x32_f16 v[80:83], v[218:221], v[202:205], v[80:83]
	v_mfma_f32_16x16x32_f16 v[104:107], v[218:221], v[210:213], v[104:107]
	v_mfma_f32_16x16x32_f16 v[108:111], v[238:241], v[202:205], v[108:111]
	v_mfma_f32_16x16x32_f16 v[112:115], v[238:241], v[206:209], v[112:115]
	v_mfma_f32_16x16x32_f16 v[116:119], v[238:241], v[210:213], v[116:119]
	v_mfma_f32_16x16x32_f16 v[230:233], v[218:221], v[206:209], v[230:233]
	v_mfma_f32_16x16x32_f16 v[218:221], v[218:221], v[214:217], v[222:225]
	v_mfma_f32_16x16x32_f16 v[222:225], v[238:241], v[214:217], v[226:229]
	s_setprio 0
	s_nop 1
	ds_read_b128 v[226:229], v129 offset:4096
	ds_read_b128 v[238:241], v129 offset:6144
	v_readfirstlane_b32 s1, v96
	v_lshl_add_u64 v[198:199], v[92:93], 0, s[58:59]
	s_mov_b32 m0, s1
	v_cvt_pk_f16_f32 v7, v6, v7
	global_load_lds_dwordx4 v[198:199], off
	v_cvt_pk_f16_f32 v6, v4, v5
	ds_write_b64 v100, v[6:7] offset:36864
	s_add_u32 s70, s22, 0x20f00
	s_addc_u32 s71, s90, 0
	global_load_dwordx4 v[4:7], v201, s[70:71] nt
	s_setprio 1
	s_waitcnt lgkmcnt(1)
	v_mfma_f32_16x16x32_f16 v[68:71], v[226:229], v[202:205], v[68:71]
	v_mfma_f32_16x16x32_f16 v[64:67], v[226:229], v[206:209], v[64:67]
	v_mfma_f32_16x16x32_f16 v[84:87], v[226:229], v[210:213], v[84:87]
	v_mfma_f32_16x16x32_f16 v[120:123], v[226:229], v[214:217], v[120:123]
	v_mfma_f32_16x16x32_f16 v[124:127], v[238:241], v[202:205], v[124:127]
	v_mfma_f32_16x16x32_f16 v[134:137], v[238:241], v[214:217], v[134:137]
	v_mfma_f32_16x16x32_f16 v[138:141], v[238:241], v[206:209], v[138:141]
	v_mfma_f32_16x16x32_f16 v[142:145], v[238:241], v[210:213], v[142:145]
	s_setprio 0
	ds_read_b128 v[226:229], v129 offset:8192
	ds_read_b128 v[238:241], v129 offset:10240
	v_readfirstlane_b32 s70, v97
	v_lshl_add_u64 v[198:199], v[92:93], 0, s[60:61]
	s_mov_b32 m0, s70
	v_cvt_pk_f16_f32 v15, v14, v15
	global_load_lds_dwordx4 v[198:199], off
	v_cvt_pk_f16_f32 v14, v12, v13
	ds_write_b64 v100, v[14:15] offset:40960
	s_add_u32 s72, s22, 0x40f00
	s_addc_u32 s73, s90, 0
	global_load_dwordx4 v[12:15], v201, s[72:73] nt
	s_setprio 1
	s_waitcnt lgkmcnt(1)
	v_mfma_f32_16x16x32_f16 v[72:75], v[226:229], v[202:205], v[72:75]
	v_mfma_f32_16x16x32_f16 v[88:91], v[226:229], v[206:209], v[88:91]
	v_mfma_f32_16x16x32_f16 v[146:149], v[226:229], v[214:217], v[146:149]
	v_mfma_f32_16x16x32_f16 v[170:173], v[226:229], v[210:213], v[170:173]
	v_mfma_f32_16x16x32_f16 v[150:153], v[238:241], v[202:205], v[150:153]
	v_mfma_f32_16x16x32_f16 v[162:165], v[238:241], v[206:209], v[162:165]
	v_mfma_f32_16x16x32_f16 v[174:177], v[238:241], v[210:213], v[174:177]
	v_mfma_f32_16x16x32_f16 v[154:157], v[238:241], v[214:217], v[154:157]
	s_setprio 0
	ds_read_b128 v[226:229], v129 offset:12288
	ds_read_b128 v[238:241], v129 offset:14336
	v_readfirstlane_b32 s71, v98
	v_lshl_add_u64 v[92:93], v[92:93], 0, s[62:63]
	s_mov_b32 m0, s71
	v_cvt_pk_f16_f32 v19, v18, v19
	global_load_lds_dwordx4 v[92:93], off
	v_cvt_pk_f16_f32 v18, v16, v17
	ds_write_b64 v100, v[18:19] offset:45056
	s_add_u32 s72, s22, 0x60f00
	s_addc_u32 s73, s90, 0
	global_load_dwordx4 v[16:19], v201, s[72:73] nt
	s_setprio 1
	s_waitcnt lgkmcnt(1)
	v_mfma_f32_16x16x32_f16 v[76:79], v[226:229], v[202:205], v[76:79]
	v_mfma_f32_16x16x32_f16 v[234:237], v[226:229], v[206:209], v[234:237]
	v_mfma_f32_16x16x32_f16 v[158:161], v[226:229], v[210:213], v[158:161]
	v_mfma_f32_16x16x32_f16 v[166:169], v[226:229], v[214:217], v[166:169]
	v_mfma_f32_16x16x32_f16 v[178:181], v[238:241], v[202:205], v[178:181]
	v_mfma_f32_16x16x32_f16 v[182:185], v[238:241], v[206:209], v[182:185]
	v_mfma_f32_16x16x32_f16 v[190:193], v[238:241], v[210:213], v[190:193]
	v_mfma_f32_16x16x32_f16 v[186:189], v[238:241], v[214:217], v[186:189]
	s_setprio 0
	ds_read_b128 v[202:205], v128
	ds_read_b128 v[206:209], v128 offset:2048
	ds_read_b128 v[210:213], v128 offset:4096
	ds_read_b128 v[214:217], v128 offset:6144
	ds_read_b128 v[226:229], v130
	ds_read_b128 v[238:241], v130 offset:2048
	v_cvt_pk_f16_f32 v23, v22, v23
	v_cvt_pk_f16_f32 v22, v20, v21
	ds_write_b64 v100, v[22:23] offset:49152
	s_add_u32 s72, s22, 0x80f00
	s_addc_u32 s73, s90, 0
	global_load_dwordx4 v[20:23], v201, s[72:73] nt
	s_setprio 1
	s_waitcnt lgkmcnt(1)
	v_mfma_f32_16x16x32_f16 v[80:83], v[226:229], v[202:205], v[80:83]
	v_mfma_f32_16x16x32_f16 v[104:107], v[226:229], v[210:213], v[104:107]
	v_mfma_f32_16x16x32_f16 v[108:111], v[238:241], v[202:205], v[108:111]
	v_mfma_f32_16x16x32_f16 v[112:115], v[238:241], v[206:209], v[112:115]
	v_mfma_f32_16x16x32_f16 v[116:119], v[238:241], v[210:213], v[116:119]
	v_mfma_f32_16x16x32_f16 v[230:233], v[226:229], v[206:209], v[230:233]
	v_mfma_f32_16x16x32_f16 v[218:221], v[226:229], v[214:217], v[218:221]
	v_mfma_f32_16x16x32_f16 v[222:225], v[238:241], v[214:217], v[222:225]
	s_setprio 0
	ds_read_b128 v[226:229], v130 offset:4096
	ds_read_b128 v[238:241], v130 offset:6144
	v_cvt_pk_f16_f32 v27, v26, v27
	v_cvt_pk_f16_f32 v26, v24, v25
	ds_write_b64 v100, v[26:27] offset:53248
	s_add_u32 s72, s22, 0xa0f00
	s_addc_u32 s73, s90, 0
	global_load_dwordx4 v[24:27], v201, s[72:73] nt
	s_setprio 1
	s_waitcnt lgkmcnt(1)
	v_mfma_f32_16x16x32_f16 v[68:71], v[226:229], v[202:205], v[68:71]
	v_mfma_f32_16x16x32_f16 v[64:67], v[226:229], v[206:209], v[64:67]
	v_mfma_f32_16x16x32_f16 v[84:87], v[226:229], v[210:213], v[84:87]
	v_mfma_f32_16x16x32_f16 v[120:123], v[226:229], v[214:217], v[120:123]
	v_mfma_f32_16x16x32_f16 v[124:127], v[238:241], v[202:205], v[124:127]
	v_mfma_f32_16x16x32_f16 v[134:137], v[238:241], v[214:217], v[134:137]
	v_mfma_f32_16x16x32_f16 v[138:141], v[238:241], v[206:209], v[138:141]
	v_mfma_f32_16x16x32_f16 v[142:145], v[238:241], v[210:213], v[142:145]
	s_setprio 0
	ds_read_b128 v[226:229], v130 offset:8192
	ds_read_b128 v[238:241], v130 offset:10240
	v_cvt_pk_f16_f32 v31, v30, v31
	v_cvt_pk_f16_f32 v30, v28, v29
	ds_write_b64 v100, v[30:31] offset:57344
	s_add_u32 s72, s22, 0xc0f00
	s_addc_u32 s73, s90, 0
	global_load_dwordx4 v[28:31], v201, s[72:73] nt
	s_setprio 1
	s_waitcnt lgkmcnt(1)
	v_mfma_f32_16x16x32_f16 v[72:75], v[226:229], v[202:205], v[72:75]
	v_mfma_f32_16x16x32_f16 v[88:91], v[226:229], v[206:209], v[88:91]
	v_mfma_f32_16x16x32_f16 v[146:149], v[226:229], v[214:217], v[146:149]
	v_mfma_f32_16x16x32_f16 v[170:173], v[226:229], v[210:213], v[170:173]
	v_mfma_f32_16x16x32_f16 v[150:153], v[238:241], v[202:205], v[150:153]
	v_mfma_f32_16x16x32_f16 v[162:165], v[238:241], v[206:209], v[162:165]
	v_mfma_f32_16x16x32_f16 v[174:177], v[238:241], v[210:213], v[174:177]
	v_mfma_f32_16x16x32_f16 v[154:157], v[238:241], v[214:217], v[154:157]
	s_setprio 0
	ds_read_b128 v[226:229], v130 offset:12288
	ds_read_b128 v[238:241], v130 offset:14336
	v_cvt_pk_f16_f32 v35, v34, v35
	v_cvt_pk_f16_f32 v34, v32, v33
	ds_write_b64 v100, v[34:35] offset:61440
	s_add_u32 s72, s22, 0xe0f00
	s_addc_u32 s73, s90, 0
	global_load_dwordx4 v[32:35], v201, s[72:73] nt
	s_setprio 1
	s_waitcnt lgkmcnt(1)
	v_mfma_f32_16x16x32_f16 v[76:79], v[226:229], v[202:205], v[76:79]
	v_mfma_f32_16x16x32_f16 v[234:237], v[226:229], v[206:209], v[234:237]
	v_mfma_f32_16x16x32_f16 v[158:161], v[226:229], v[210:213], v[158:161]
	v_mfma_f32_16x16x32_f16 v[166:169], v[226:229], v[214:217], v[166:169]
	v_mfma_f32_16x16x32_f16 v[178:181], v[238:241], v[202:205], v[178:181]
	v_mfma_f32_16x16x32_f16 v[182:185], v[238:241], v[206:209], v[182:185]
	v_mfma_f32_16x16x32_f16 v[190:193], v[238:241], v[210:213], v[190:193]
	v_mfma_f32_16x16x32_f16 v[186:189], v[238:241], v[214:217], v[186:189]
	s_setprio 0
	s_waitcnt vmcnt(4)
	s_waitcnt lgkmcnt(0)
	s_barrier
	ds_read_b128 v[202:205], v131 offset:32768
	ds_read_b128 v[206:209], v131 offset:34816
	ds_read_b128 v[210:213], v131 offset:36864
	ds_read_b128 v[214:217], v131 offset:38912
	ds_read_b128 v[226:229], v129 offset:32768
	ds_read_b128 v[238:241], v129 offset:34816
	v_lshl_add_u64 v[198:199], s[54:55], 0, v[196:197]
	v_readfirstlane_b32 s64, v94
	s_mov_b32 m0, s64
	v_cvt_pk_f16_f32 v11, v10, v11
	global_load_lds_dwordx4 v[198:199], off
	v_cvt_pk_f16_f32 v10, v8, v9
	ds_write_b64 v100, v[10:11]
	s_setprio 1
	s_waitcnt lgkmcnt(1)
	v_mfma_f32_16x16x32_f16 v[8:11], v[226:229], v[202:205], v[80:83]
	v_mfma_f32_16x16x32_f16 v[80:83], v[226:229], v[206:209], v[230:233]
	v_mfma_f32_16x16x32_f16 v[92:95], v[226:229], v[210:213], v[104:107]
	v_mfma_f32_16x16x32_f16 v[104:107], v[226:229], v[214:217], v[218:221]
	v_mfma_f32_16x16x32_f16 v[108:111], v[238:241], v[202:205], v[108:111]
	v_mfma_f32_16x16x32_f16 v[112:115], v[238:241], v[206:209], v[112:115]
	v_mfma_f32_16x16x32_f16 v[116:119], v[238:241], v[210:213], v[116:119]
	v_mfma_f32_16x16x32_f16 v[218:221], v[238:241], v[214:217], v[222:225]
	s_setprio 0
	s_nop 1
	ds_read_b128 v[222:225], v129 offset:36864
	ds_read_b128 v[226:229], v129 offset:38912
	v_readfirstlane_b32 s64, v99
	v_lshl_add_u64 v[96:97], v[198:199], 0, s[58:59]
	s_mov_b32 m0, s64
	v_cvt_pk_f16_f32 v43, v42, v43
	global_load_lds_dwordx4 v[96:97], off
	v_cvt_pk_f16_f32 v42, v40, v41
	ds_write_b64 v100, v[42:43] offset:4096
	s_setprio 1
	s_waitcnt lgkmcnt(1)
	v_mfma_f32_16x16x32_f16 v[40:43], v[222:225], v[202:205], v[68:71]
	v_mfma_f32_16x16x32_f16 v[64:67], v[222:225], v[206:209], v[64:67]
	v_mfma_f32_16x16x32_f16 v[68:71], v[222:225], v[210:213], v[84:87]
	v_mfma_f32_16x16x32_f16 v[84:87], v[222:225], v[214:217], v[120:123]
	v_mfma_f32_16x16x32_f16 v[96:99], v[226:229], v[202:205], v[124:127]
	v_mfma_f32_16x16x32_f16 v[120:123], v[226:229], v[206:209], v[138:141]
	v_mfma_f32_16x16x32_f16 v[124:127], v[226:229], v[210:213], v[142:145]
	v_mfma_f32_16x16x32_f16 v[134:137], v[226:229], v[214:217], v[134:137]
	s_setprio 0
	ds_read_b128 v[138:141], v129 offset:40960
	ds_read_b128 v[142:145], v129 offset:43008
	v_readfirstlane_b32 s64, v101
	v_lshl_add_u64 v[222:223], v[198:199], 0, s[60:61]
	s_mov_b32 m0, s64
	v_cvt_pk_f16_f32 v47, v46, v47
	global_load_lds_dwordx4 v[222:223], off
	v_cvt_pk_f16_f32 v46, v44, v45
	ds_write_b64 v100, v[46:47] offset:8192
	s_setprio 1
	s_waitcnt lgkmcnt(1)
	v_mfma_f32_16x16x32_f16 v[44:47], v[138:141], v[202:205], v[72:75]
	v_mfma_f32_16x16x32_f16 v[72:75], v[138:141], v[206:209], v[88:91]
	v_mfma_f32_16x16x32_f16 v[88:91], v[138:141], v[210:213], v[170:173]
	v_mfma_f32_16x16x32_f16 v[138:141], v[138:141], v[214:217], v[146:149]
	v_mfma_f32_16x16x32_f16 v[146:149], v[142:145], v[202:205], v[150:153]
	v_mfma_f32_16x16x32_f16 v[150:153], v[142:145], v[206:209], v[162:165]
	v_mfma_f32_16x16x32_f16 v[162:165], v[142:145], v[210:213], v[174:177]
	v_mfma_f32_16x16x32_f16 v[142:145], v[142:145], v[214:217], v[154:157]
	s_setprio 0
	s_nop 1
	ds_read_b128 v[154:157], v129 offset:45056
	ds_read_b128 v[170:173], v129 offset:47104
	v_readfirstlane_b32 s64, v102
	v_lshl_add_u64 v[174:175], v[198:199], 0, s[62:63]
	s_mov_b32 m0, s64
	v_cvt_pk_f16_f32 v51, v50, v51
	global_load_lds_dwordx4 v[174:175], off
	v_cvt_pk_f16_f32 v50, v48, v49
	ds_write_b64 v100, v[50:51] offset:12288
	s_setprio 1
	s_waitcnt lgkmcnt(1)
	v_mfma_f32_16x16x32_f16 v[48:51], v[154:157], v[202:205], v[76:79]
	v_mfma_f32_16x16x32_f16 v[76:79], v[154:157], v[206:209], v[234:237]
	v_mfma_f32_16x16x32_f16 v[158:161], v[154:157], v[210:213], v[158:161]
	v_mfma_f32_16x16x32_f16 v[154:157], v[154:157], v[214:217], v[166:169]
	v_mfma_f32_16x16x32_f16 v[166:169], v[170:173], v[202:205], v[178:181]
	v_mfma_f32_16x16x32_f16 v[174:177], v[170:173], v[206:209], v[182:185]
	v_mfma_f32_16x16x32_f16 v[178:181], v[170:173], v[210:213], v[190:193]
	v_mfma_f32_16x16x32_f16 v[170:173], v[170:173], v[214:217], v[186:189]
	s_setprio 0
	ds_read_b128 v[182:185], v128 offset:32768
	s_nop 0
	ds_read_b128 v[186:189], v128 offset:34816
	ds_read_b128 v[190:193], v128 offset:36864
	ds_read_b128 v[202:205], v128 offset:38912
	ds_read_b128 v[206:209], v130 offset:32768
	ds_read_b128 v[210:213], v130 offset:34816
	v_cvt_pk_f16_f32 v55, v54, v55
	v_cvt_pk_f16_f32 v54, v52, v53
	ds_write_b64 v100, v[54:55] offset:16384
	s_setprio 1
	s_waitcnt lgkmcnt(1)
	v_mfma_f32_16x16x32_f16 v[8:11], v[206:209], v[182:185], v[8:11]
	v_mfma_f32_16x16x32_f16 v[52:55], v[206:209], v[186:189], v[80:83]
	v_mfma_f32_16x16x32_f16 v[80:83], v[206:209], v[190:193], v[92:95]
	v_mfma_f32_16x16x32_f16 v[92:95], v[206:209], v[202:205], v[104:107]
	v_mfma_f32_16x16x32_f16 v[102:105], v[210:213], v[182:185], v[108:111]
	v_mfma_f32_16x16x32_f16 v[106:109], v[210:213], v[186:189], v[112:115]
	v_mfma_f32_16x16x32_f16 v[110:113], v[210:213], v[190:193], v[116:119]
	v_mfma_f32_16x16x32_f16 v[114:117], v[210:213], v[202:205], v[218:221]
	s_setprio 0
	ds_read_b128 v[206:209], v130 offset:36864
	ds_read_b128 v[210:213], v130 offset:38912
	v_cvt_pk_f16_f32 v59, v58, v59
	v_cvt_pk_f16_f32 v58, v56, v57
	ds_write_b64 v100, v[58:59] offset:20480
	s_setprio 1
	s_waitcnt lgkmcnt(1)
	v_mfma_f32_16x16x32_f16 v[40:43], v[206:209], v[182:185], v[40:43]
	v_mfma_f32_16x16x32_f16 v[56:59], v[206:209], v[186:189], v[64:67]
	v_mfma_f32_16x16x32_f16 v[64:67], v[206:209], v[190:193], v[68:71]
	v_mfma_f32_16x16x32_f16 v[68:71], v[206:209], v[202:205], v[84:87]
	v_mfma_f32_16x16x32_f16 v[84:87], v[210:213], v[182:185], v[96:99]
	v_mfma_f32_16x16x32_f16 v[96:99], v[210:213], v[186:189], v[120:123]
	v_mfma_f32_16x16x32_f16 v[118:121], v[210:213], v[190:193], v[124:127]
	v_mfma_f32_16x16x32_f16 v[122:125], v[210:213], v[202:205], v[134:137]
	s_setprio 0
	s_nop 1
	ds_read_b128 v[134:137], v130 offset:40960
	ds_read_b128 v[206:209], v130 offset:43008
	v_cvt_pk_f16_f32 v63, v62, v63
	v_cvt_pk_f16_f32 v62, v60, v61
	ds_write_b64 v100, v[62:63] offset:24576
	s_setprio 1
	s_waitcnt lgkmcnt(1)
	v_mfma_f32_16x16x32_f16 v[44:47], v[134:137], v[182:185], v[44:47]
	v_mfma_f32_16x16x32_f16 v[60:63], v[134:137], v[186:189], v[72:75]
	v_mfma_f32_16x16x32_f16 v[72:75], v[134:137], v[190:193], v[88:91]
	v_mfma_f32_16x16x32_f16 v[88:91], v[134:137], v[202:205], v[138:141]
	v_mfma_f32_16x16x32_f16 v[134:137], v[206:209], v[182:185], v[146:149]
	v_mfma_f32_16x16x32_f16 v[146:149], v[206:209], v[190:193], v[162:165]
	v_mfma_f32_16x16x32_f16 v[138:141], v[206:209], v[186:189], v[150:153]
	v_mfma_f32_16x16x32_f16 v[142:145], v[206:209], v[202:205], v[142:145]
	s_setprio 0
	s_nop 0
	ds_read_b128 v[150:153], v130 offset:45056
	ds_read_b128 v[162:165], v130 offset:47104
	v_cvt_pk_f16_f32 v39, v38, v39
	v_cvt_pk_f16_f32 v38, v36, v37
	ds_write_b64 v100, v[38:39] offset:28672
	s_setprio 1
	s_waitcnt lgkmcnt(1)
	v_mfma_f32_16x16x32_f16 v[36:39], v[150:153], v[182:185], v[48:51]
	v_mfma_f32_16x16x32_f16 v[48:51], v[150:153], v[186:189], v[76:79]
	v_mfma_f32_16x16x32_f16 v[76:79], v[150:153], v[190:193], v[158:161]
	v_mfma_f32_16x16x32_f16 v[150:153], v[150:153], v[202:205], v[154:157]
	v_mfma_f32_16x16x32_f16 v[154:157], v[162:165], v[182:185], v[166:169]
	v_mfma_f32_16x16x32_f16 v[158:161], v[162:165], v[186:189], v[174:177]
	v_mfma_f32_16x16x32_f16 v[166:169], v[162:165], v[190:193], v[178:181]
	v_mfma_f32_16x16x32_f16 v[162:165], v[162:165], v[202:205], v[170:173]
	s_setprio 0
	s_waitcnt vmcnt(0)
	s_waitcnt lgkmcnt(0)
	s_barrier
	s_nop 0
	ds_read_b128 v[170:173], v131
	ds_read_b128 v[174:177], v131 offset:2048
	ds_read_b128 v[178:181], v131 offset:4096
	ds_read_b128 v[182:185], v131 offset:6144
	ds_read_b128 v[186:189], v129
	ds_read_b128 v[190:193], v129 offset:2048
	v_lshl_add_u64 v[126:127], s[56:57], 0, v[196:197]
	s_mov_b32 m0, s0
	v_cvt_pk_f16_f32 v3, v2, v3
	global_load_lds_dwordx4 v[126:127], off
	v_cvt_pk_f16_f32 v2, v0, v1
	ds_write_b64 v100, v[2:3] offset:32768
	s_setprio 1
	s_waitcnt lgkmcnt(1)
	v_mfma_f32_16x16x32_f16 v[0:3], v[186:189], v[170:173], v[8:11]
	v_mfma_f32_16x16x32_f16 v[8:11], v[186:189], v[174:177], v[52:55]
	v_mfma_f32_16x16x32_f16 v[52:55], v[186:189], v[178:181], v[80:83]
	v_mfma_f32_16x16x32_f16 v[80:83], v[186:189], v[182:185], v[92:95]
	v_mfma_f32_16x16x32_f16 v[92:95], v[190:193], v[170:173], v[102:105]
	v_mfma_f32_16x16x32_f16 v[102:105], v[190:193], v[174:177], v[106:109]
	v_mfma_f32_16x16x32_f16 v[106:109], v[190:193], v[178:181], v[110:113]
	v_mfma_f32_16x16x32_f16 v[110:113], v[190:193], v[182:185], v[114:117]
	s_setprio 0
	s_nop 1
	ds_read_b128 v[114:117], v129 offset:4096
	ds_read_b128 v[186:189], v129 offset:6144
	s_mov_b32 m0, s1
	v_lshl_add_u64 v[190:191], v[126:127], 0, s[58:59]
	global_load_lds_dwordx4 v[190:191], off
	v_cvt_pk_f16_f32 v7, v6, v7
	v_cvt_pk_f16_f32 v6, v4, v5
	ds_write_b64 v100, v[6:7] offset:36864
	s_setprio 1
	s_waitcnt lgkmcnt(1)
	v_mfma_f32_16x16x32_f16 v[190:193], v[114:117], v[170:173], v[40:43]
	v_mfma_f32_16x16x32_f16 v[56:59], v[114:117], v[174:177], v[56:59]
	v_mfma_f32_16x16x32_f16 v[64:67], v[114:117], v[178:181], v[64:67]
	v_mfma_f32_16x16x32_f16 v[68:71], v[114:117], v[182:185], v[68:71]
	v_mfma_f32_16x16x32_f16 v[84:87], v[186:189], v[170:173], v[84:87]
	v_mfma_f32_16x16x32_f16 v[96:99], v[186:189], v[174:177], v[96:99]
	v_mfma_f32_16x16x32_f16 v[114:117], v[186:189], v[178:181], v[118:121]
	v_mfma_f32_16x16x32_f16 v[118:121], v[186:189], v[182:185], v[122:125]
	s_setprio 0
	ds_read_b128 v[4:7], v129 offset:8192
	ds_read_b128 v[40:43], v129 offset:10240
	s_mov_b32 m0, s70
	v_lshl_add_u64 v[122:123], v[126:127], 0, s[60:61]
	global_load_lds_dwordx4 v[122:123], off
	v_cvt_pk_f16_f32 v15, v14, v15
	v_cvt_pk_f16_f32 v14, v12, v13
	ds_write_b64 v100, v[14:15] offset:40960
	s_setprio 1
	s_waitcnt lgkmcnt(1)
	v_mfma_f32_16x16x32_f16 v[122:125], v[4:7], v[170:173], v[44:47]
	v_mfma_f32_16x16x32_f16 v[88:91], v[4:7], v[182:185], v[88:91]
	v_mfma_f32_16x16x32_f16 v[134:137], v[40:43], v[170:173], v[134:137]
	v_mfma_f32_16x16x32_f16 v[146:149], v[40:43], v[178:181], v[146:149]
	v_mfma_f32_16x16x32_f16 v[186:189], v[4:7], v[174:177], v[60:63]
	v_mfma_f32_16x16x32_f16 v[202:205], v[4:7], v[178:181], v[72:75]
	v_mfma_f32_16x16x32_f16 v[138:141], v[40:43], v[174:177], v[138:141]
	v_mfma_f32_16x16x32_f16 v[142:145], v[40:43], v[182:185], v[142:145]
	s_setprio 0
	ds_read_b128 v[4:7], v129 offset:12288
	ds_read_b128 v[12:15], v129 offset:14336
	s_mov_b32 m0, s71
	v_lshl_add_u64 v[40:41], v[126:127], 0, s[62:63]
	global_load_lds_dwordx4 v[40:41], off
	v_cvt_pk_f16_f32 v19, v18, v19
	v_cvt_pk_f16_f32 v18, v16, v17
	ds_write_b64 v100, v[18:19] offset:45056
	s_setprio 1
	s_waitcnt lgkmcnt(1)
	v_mfma_f32_16x16x32_f16 v[206:209], v[4:7], v[170:173], v[36:39]
	v_mfma_f32_16x16x32_f16 v[210:213], v[4:7], v[174:177], v[48:51]
	v_mfma_f32_16x16x32_f16 v[214:217], v[4:7], v[178:181], v[76:79]
	v_mfma_f32_16x16x32_f16 v[150:153], v[4:7], v[182:185], v[150:153]
	v_mfma_f32_16x16x32_f16 v[154:157], v[12:15], v[170:173], v[154:157]
	v_mfma_f32_16x16x32_f16 v[158:161], v[12:15], v[174:177], v[158:161]
	v_mfma_f32_16x16x32_f16 v[166:169], v[12:15], v[178:181], v[166:169]
	v_mfma_f32_16x16x32_f16 v[162:165], v[12:15], v[182:185], v[162:165]
	s_setprio 0
	ds_read_b128 v[170:173], v128
	ds_read_b128 v[174:177], v128 offset:2048
	ds_read_b128 v[178:181], v128 offset:4096
	ds_read_b128 v[182:185], v128 offset:6144
	ds_read_b128 v[12:15], v130
	ds_read_b128 v[40:43], v130 offset:2048
	v_cvt_pk_f16_f32 v5, v22, v23
	v_cvt_pk_f16_f32 v4, v20, v21
	ds_write_b64 v100, v[4:5] offset:49152
	s_setprio 1
	s_waitcnt lgkmcnt(1)
	v_mfma_f32_16x16x32_f16 v[0:3], v[12:15], v[170:173], v[0:3]
	v_mfma_f32_16x16x32_f16 v[4:7], v[12:15], v[174:177], v[8:11]
	v_mfma_f32_16x16x32_f16 v[8:11], v[12:15], v[178:181], v[52:55]
	v_mfma_f32_16x16x32_f16 v[12:15], v[12:15], v[182:185], v[80:83]
	v_mfma_f32_16x16x32_f16 v[16:19], v[40:43], v[170:173], v[92:95]
	v_mfma_f32_16x16x32_f16 v[20:23], v[40:43], v[174:177], v[102:105]
	v_mfma_f32_16x16x32_f16 v[36:39], v[40:43], v[178:181], v[106:109]
	v_mfma_f32_16x16x32_f16 v[40:43], v[40:43], v[182:185], v[110:113]
	s_setprio 0
	ds_read_b128 v[52:55], v130 offset:4096
	ds_read_b128 v[72:75], v130 offset:6144
	v_cvt_pk_f16_f32 v27, v26, v27
	v_cvt_pk_f16_f32 v26, v24, v25
	ds_write_b64 v100, v[26:27] offset:53248
	s_setprio 1
	s_waitcnt lgkmcnt(1)
	v_mfma_f32_16x16x32_f16 v[24:27], v[52:55], v[170:173], v[190:193]
	v_mfma_f32_16x16x32_f16 v[44:47], v[52:55], v[174:177], v[56:59]
	v_mfma_f32_16x16x32_f16 v[48:51], v[52:55], v[178:181], v[64:67]
	v_mfma_f32_16x16x32_f16 v[52:55], v[52:55], v[182:185], v[68:71]
	v_mfma_f32_16x16x32_f16 v[56:59], v[72:75], v[170:173], v[84:87]
	v_mfma_f32_16x16x32_f16 v[60:63], v[72:75], v[174:177], v[96:99]
	v_mfma_f32_16x16x32_f16 v[64:67], v[72:75], v[178:181], v[114:117]
	v_mfma_f32_16x16x32_f16 v[68:71], v[72:75], v[182:185], v[118:121]
	s_setprio 0
	ds_read_b128 v[80:83], v130 offset:8192
	ds_read_b128 v[96:99], v130 offset:10240
	v_cvt_pk_f16_f32 v31, v30, v31
	v_cvt_pk_f16_f32 v30, v28, v29
	ds_write_b64 v100, v[30:31] offset:57344
	s_setprio 1
	s_waitcnt lgkmcnt(1)
	v_mfma_f32_16x16x32_f16 v[28:31], v[80:83], v[170:173], v[122:125]
	v_mfma_f32_16x16x32_f16 v[72:75], v[80:83], v[174:177], v[186:189]
	v_mfma_f32_16x16x32_f16 v[76:79], v[80:83], v[178:181], v[202:205]
	v_mfma_f32_16x16x32_f16 v[80:83], v[80:83], v[182:185], v[88:91]
	v_mfma_f32_16x16x32_f16 v[84:87], v[96:99], v[170:173], v[134:137]
	v_mfma_f32_16x16x32_f16 v[88:91], v[96:99], v[174:177], v[138:141]
	v_mfma_f32_16x16x32_f16 v[92:95], v[96:99], v[178:181], v[146:149]
	v_mfma_f32_16x16x32_f16 v[96:99], v[96:99], v[182:185], v[142:145]
	s_setprio 0
	ds_read_b128 v[108:111], v130 offset:12288
	ds_read_b128 v[124:127], v130 offset:14336
	v_cvt_pk_f16_f32 v35, v34, v35
	v_cvt_pk_f16_f32 v34, v32, v33
	ds_write_b64 v100, v[34:35] offset:61440
	s_setprio 1
	s_waitcnt lgkmcnt(1)
	v_mfma_f32_16x16x32_f16 v[32:35], v[108:111], v[170:173], v[206:209]
	v_mfma_f32_16x16x32_f16 v[100:103], v[108:111], v[174:177], v[210:213]
	v_mfma_f32_16x16x32_f16 v[104:107], v[108:111], v[178:181], v[214:217]
	v_mfma_f32_16x16x32_f16 v[108:111], v[108:111], v[182:185], v[150:153]
	v_mfma_f32_16x16x32_f16 v[112:115], v[124:127], v[170:173], v[154:157]
	v_mfma_f32_16x16x32_f16 v[116:119], v[124:127], v[174:177], v[158:161]
	v_mfma_f32_16x16x32_f16 v[120:123], v[124:127], v[178:181], v[166:169]
	v_mfma_f32_16x16x32_f16 v[124:127], v[124:127], v[182:185], v[162:165]
	s_setprio 0
	s_waitcnt vmcnt(0)
	s_waitcnt lgkmcnt(0)
	s_barrier
	ds_read_b128 v[134:137], v131 offset:32768
	ds_read_b128 v[138:141], v131 offset:34816
	ds_read_b128 v[142:145], v131 offset:36864
	ds_read_b128 v[148:151], v131 offset:38912
	ds_read_b128 v[152:155], v129 offset:32768
	ds_read_b128 v[156:159], v129 offset:34816
	s_setprio 1
	s_waitcnt lgkmcnt(0)
	v_mfma_f32_16x16x32_f16 v[0:3], v[152:155], v[134:137], v[0:3]
	v_mfma_f32_16x16x32_f16 v[4:7], v[152:155], v[138:141], v[4:7]
	v_mfma_f32_16x16x32_f16 v[8:11], v[152:155], v[142:145], v[8:11]
	v_mfma_f32_16x16x32_f16 v[12:15], v[152:155], v[148:151], v[12:15]
	v_mfma_f32_16x16x32_f16 v[16:19], v[156:159], v[134:137], v[16:19]
	v_mfma_f32_16x16x32_f16 v[20:23], v[156:159], v[138:141], v[20:23]
	v_mfma_f32_16x16x32_f16 v[36:39], v[156:159], v[142:145], v[36:39]
	v_mfma_f32_16x16x32_f16 v[40:43], v[156:159], v[148:151], v[40:43]
	s_setprio 0
	ds_read_b128 v[152:155], v129 offset:36864
	ds_read_b128 v[156:159], v129 offset:38912
	v_and_b32_e32 v250, 0x7ffffc00, v194
	v_lshl_add_u64 v[252:253], s[10:11], 0, v[196:197]
	v_readfirstlane_b32 s32, v250
	s_nop 0
	s_mov_b32 m0, s32
	s_nop 0
	global_load_lds_dwordx4 v[252:253], off
	v_mov_b32_e32 v146, 0
	v_and_b32_e32 v251, 0xfffffff, v132
	v_cmp_gt_u32_e32 vcc, s82, v251
	v_mov_b32_e32 v132, 0
	v_mov_b32_e32 v133, 0
	s_and_saveexec_b64 s[0:1], vcc
	s_cbranch_execz .LBB1_7
	s_and_b32 s64, s78, 0x7ffffc00
	s_or_b32 s64, s64, s33
	v_or_b32_e32 v132, s64, v251
	v_mov_b32_e32 v133, v195
	v_lshl_add_u64 v[132:133], v[132:133], 2, s[12:13]
	global_load_dword v133, v[132:133], off
	v_or_b32_e32 v132, s33, v251
	v_lshlrev_b32_e32 v132, 2, v132
	global_load_dword v146, v132, s[16:17]
	s_nop 0
	global_load_dword v132, v132, s[14:15]
.LBB1_7:
	s_or_b64 exec, exec, s[0:1]
	v_lshl_add_u64 v[254:255], v[252:253], 0, s[58:59]
	s_add_u32 m0, s32, 0x2000
	s_nop 0
	global_load_lds_dwordx4 v[254:255], off
	s_setprio 1
	s_waitcnt lgkmcnt(0)
	v_mfma_f32_16x16x32_f16 v[24:27], v[152:155], v[134:137], v[24:27]
	v_mfma_f32_16x16x32_f16 v[44:47], v[152:155], v[138:141], v[44:47]
	v_mfma_f32_16x16x32_f16 v[172:175], v[156:159], v[142:145], v[64:67]
	v_mfma_f32_16x16x32_f16 v[66:69], v[156:159], v[148:151], v[68:71]
	v_mfma_f32_16x16x32_f16 v[160:163], v[152:155], v[142:145], v[48:51]
	v_mfma_f32_16x16x32_f16 v[152:155], v[152:155], v[148:151], v[52:55]
	v_mfma_f32_16x16x32_f16 v[164:167], v[156:159], v[134:137], v[56:59]
	v_mfma_f32_16x16x32_f16 v[168:171], v[156:159], v[138:141], v[60:63]
	s_setprio 0
	ds_read_b128 v[48:51], v129 offset:40960
	ds_read_b128 v[52:55], v129 offset:43008
	v_lshl_add_u64 v[254:255], v[252:253], 0, s[60:61]
	s_add_u32 m0, s32, 0x4000
	s_nop 0
	global_load_lds_dwordx4 v[254:255], off
	s_setprio 1
	s_waitcnt lgkmcnt(0)
	v_mfma_f32_16x16x32_f16 v[28:31], v[48:51], v[134:137], v[28:31]
	v_mfma_f32_16x16x32_f16 v[70:73], v[48:51], v[138:141], v[72:75]
	v_mfma_f32_16x16x32_f16 v[74:77], v[48:51], v[142:145], v[76:79]
	v_mfma_f32_16x16x32_f16 v[78:81], v[48:51], v[148:151], v[80:83]
	v_mfma_f32_16x16x32_f16 v[82:85], v[52:55], v[134:137], v[84:87]
	v_mfma_f32_16x16x32_f16 v[86:89], v[52:55], v[138:141], v[88:91]
	v_mfma_f32_16x16x32_f16 v[90:93], v[52:55], v[142:145], v[92:95]
	v_mfma_f32_16x16x32_f16 v[94:97], v[52:55], v[148:151], v[96:99]
	s_setprio 0
	ds_read_b128 v[48:51], v129 offset:45056
	ds_read_b128 v[52:55], v129 offset:47104
	v_lshl_add_u64 v[254:255], v[252:253], 0, s[62:63]
	s_add_u32 m0, s32, 0x6000
	s_nop 0
	global_load_lds_dwordx4 v[254:255], off
	s_setprio 1
	s_waitcnt lgkmcnt(0)
	v_mfma_f32_16x16x32_f16 v[202:205], v[52:55], v[138:141], v[116:119]
	v_mfma_f32_16x16x32_f16 v[206:209], v[52:55], v[142:145], v[120:123]
	v_mfma_f32_16x16x32_f16 v[156:159], v[48:51], v[134:137], v[32:35]
	v_mfma_f32_16x16x32_f16 v[176:179], v[48:51], v[138:141], v[100:103]
	v_mfma_f32_16x16x32_f16 v[180:183], v[48:51], v[142:145], v[104:107]
	v_mfma_f32_16x16x32_f16 v[184:187], v[48:51], v[148:151], v[108:111]
	v_mfma_f32_16x16x32_f16 v[188:191], v[52:55], v[134:137], v[112:115]
	v_mfma_f32_16x16x32_f16 v[148:151], v[52:55], v[148:151], v[124:127]
	s_setprio 0
	ds_read_b128 v[210:213], v128 offset:32768
	ds_read_b128 v[214:217], v128 offset:34816
	ds_read_b128 v[218:221], v128 offset:36864
	ds_read_b128 v[222:225], v128 offset:38912
	ds_read_b128 v[32:35], v130 offset:32768
	ds_read_b128 v[98:101], v130 offset:34816
	s_mov_b64 s[100:101], 0x8000
	v_lshl_add_u64 v[254:255], v[252:253], 0, s[100:101]
	s_add_u32 m0, s32, 0x10000
	s_nop 0
	global_load_lds_dwordx4 v[254:255], off
	s_setprio 1
	s_waitcnt lgkmcnt(0)
	v_mfma_f32_16x16x32_f16 v[50:53], v[32:35], v[210:213], v[0:3]
	v_mfma_f32_16x16x32_f16 v[54:57], v[32:35], v[214:217], v[4:7]
	v_mfma_f32_16x16x32_f16 v[58:61], v[32:35], v[218:221], v[8:11]
	v_mfma_f32_16x16x32_f16 v[62:65], v[32:35], v[222:225], v[12:15]
	v_mfma_f32_16x16x32_f16 v[142:145], v[98:101], v[210:213], v[16:19]
	v_mfma_f32_16x16x32_f16 v[138:141], v[98:101], v[214:217], v[20:23]
	v_mfma_f32_16x16x32_f16 v[134:137], v[98:101], v[218:221], v[36:39]
	v_mfma_f32_16x16x32_f16 v[126:129], v[98:101], v[222:225], v[40:43]
	s_setprio 0
	ds_read_b128 v[0:3], v130 offset:36864
	ds_read_b128 v[4:7], v130 offset:38912
	s_mov_b64 s[100:101], 0xa000
	v_lshl_add_u64 v[254:255], v[252:253], 0, s[100:101]
	s_add_u32 m0, s32, 0x12000
	s_nop 0
	global_load_lds_dwordx4 v[254:255], off
	s_setprio 1
	s_waitcnt lgkmcnt(0)
	v_mfma_f32_16x16x32_f16 v[34:37], v[0:3], v[210:213], v[24:27]
	v_mfma_f32_16x16x32_f16 v[38:41], v[0:3], v[214:217], v[44:47]
	v_mfma_f32_16x16x32_f16 v[42:45], v[0:3], v[218:221], v[160:163]
	v_mfma_f32_16x16x32_f16 v[46:49], v[0:3], v[222:225], v[152:155]
	v_mfma_f32_16x16x32_f16 v[122:125], v[4:7], v[210:213], v[164:167]
	v_mfma_f32_16x16x32_f16 v[118:121], v[4:7], v[214:217], v[168:171]
	v_mfma_f32_16x16x32_f16 v[114:117], v[4:7], v[218:221], v[172:175]
	v_mfma_f32_16x16x32_f16 v[110:113], v[4:7], v[222:225], v[66:69]
	s_setprio 0
	ds_read_b128 v[10:13], v130 offset:40960
	ds_read_b128 v[18:21], v130 offset:43008
	v_lshl_add_u64 v[254:255], v[252:253], 0, s[66:67]
	s_add_u32 m0, s32, 0x14000
	s_nop 0
	global_load_lds_dwordx4 v[254:255], off
	s_setprio 1
	s_waitcnt lgkmcnt(0)
	v_mfma_f32_16x16x32_f16 v[2:5], v[10:13], v[210:213], v[28:31]
	v_mfma_f32_16x16x32_f16 v[6:9], v[10:13], v[214:217], v[70:73]
	v_mfma_f32_16x16x32_f16 v[14:17], v[10:13], v[218:221], v[74:77]
	v_mfma_f32_16x16x32_f16 v[30:33], v[10:13], v[222:225], v[78:81]
	v_mfma_f32_16x16x32_f16 v[106:109], v[18:21], v[210:213], v[82:85]
	v_mfma_f32_16x16x32_f16 v[102:105], v[18:21], v[214:217], v[86:89]
	v_mfma_f32_16x16x32_f16 v[98:101], v[18:21], v[218:221], v[90:93]
	v_mfma_f32_16x16x32_f16 v[86:89], v[18:21], v[222:225], v[94:97]
	s_setprio 0
	ds_read_b128 v[26:29], v130 offset:45056
	ds_read_b128 v[66:69], v130 offset:47104
	v_lshl_add_u64 v[254:255], v[252:253], 0, s[68:69]
	s_add_u32 m0, s32, 0x16000
	s_nop 0
	global_load_lds_dwordx4 v[254:255], off
	s_setprio 1
	s_waitcnt lgkmcnt(0)
	v_mfma_f32_16x16x32_f16 v[10:13], v[26:29], v[210:213], v[156:159]
	v_mfma_f32_16x16x32_f16 v[18:21], v[26:29], v[214:217], v[176:179]
	v_mfma_f32_16x16x32_f16 v[22:25], v[26:29], v[218:221], v[180:183]
	v_mfma_f32_16x16x32_f16 v[26:29], v[26:29], v[222:225], v[184:187]
	v_mfma_f32_16x16x32_f16 v[78:81], v[66:69], v[210:213], v[188:191]
	v_mfma_f32_16x16x32_f16 v[74:77], v[66:69], v[214:217], v[202:205]
	v_mfma_f32_16x16x32_f16 v[70:73], v[66:69], v[218:221], v[206:209]
	v_mfma_f32_16x16x32_f16 v[66:69], v[66:69], v[222:225], v[148:151]
	s_setprio 0
	s_waitcnt vmcnt(0)
	s_waitcnt lgkmcnt(0)
	s_waitcnt vmcnt(0)
	s_barrier
	v_lshrrev_b32 v0, 4, v194
	s_nop 0
	v_and_b32_e32 v204, 63, v0
	v_lshlrev_b32_e32 v82, 2, v204
	v_ashrrev_i32_e32 v1, 6, v0
	v_cmp_gt_i32_e32 vcc, s82, v0
	v_xor_b32_e32 v205, 0x80, v82
	v_xor_b32_e32 v206, 64, v82
	s_and_saveexec_b64 s[0:1], vcc
	s_cbranch_execz .LBB1_10
	v_sub_f32_e64 v83, v146, |v146|
	v_cmp_eq_u32_e32 vcc, 63, v204
	v_lshlrev_b32_e32 v85, 2, v0
	v_mul_f32_e32 v84, -2.0, v146
	s_nop 1
	v_add_f32_dpp v83, v83, v83 quad_perm:[1,0,3,2] row_mask:0xf bank_mask:0xf
	s_nop 1
	v_add_f32_dpp v83, v83, v83 quad_perm:[2,3,0,1] row_mask:0xf bank_mask:0xf
	s_nop 1
	v_add_f32_dpp v83, v83, v83 row_half_mirror row_mask:0xf bank_mask:0xf
	s_nop 1
	v_add_f32_dpp v83, v83, v83 row_mirror row_mask:0xf bank_mask:0xf
	s_nop 1
	v_add_f32_dpp v83, v83, v83 row_bcast:15 row_mask:0xa bank_mask:0xf
	s_nop 1
	v_add_f32_dpp v83, v83, v83 row_bcast:31 row_mask:0xc bank_mask:0xf
	ds_write2st64_b32 v85, v133, v84 offset0:128 offset1:132
	ds_write_b32 v85, v132 offset:34816
	v_mov_b32_e32 v82, v83
	v_lshlrev_b32_e32 v83, 2, v1
	s_and_b64 exec, exec, vcc
	s_cbranch_execz .LBB1_10
	ds_write_b32 v83, v82 offset:35840
